# v39 plus: phase-10 token indices loaded once ahead of the loop; expert-up SwiGLU epilogue re-emitted with packed f32 ops (bit-identical)
# speedup vs baseline: 1.0018x; 1.0018x over previous
_Z10hybrid_fwd4Args:
	s_mov_b32 s100, 0xbc1d265f
	s_mov_b32 s101, 0x37800000
	s_mov_b32 s99, 0
	s_load_dwordx2 s[78:79], s[0:1], 0xb0
	s_load_dwordx4 s[4:7], s[0:1], 0xa0
	s_mov_b32 s74, s2
	s_add_u32 s2, s0, 0xc0
	s_addc_u32 s3, s1, 0
	v_readfirstlane_b32 s64, v0
	s_waitcnt lgkmcnt(0)
	v_writelane_b32 v254, s4, 0
	s_mov_b32 s71, s74
	s_nop 0
	v_writelane_b32 v254, s5, 1
	v_writelane_b32 v254, s6, 2
	v_writelane_b32 v254, s7, 3
	s_load_dword s80, s[0:1], 0xc0
	s_load_dwordx8 s[4:11], s[0:1], 0x80
	s_waitcnt lgkmcnt(0)
	v_writelane_b32 v254, s4, 4
	s_nop 1
	v_writelane_b32 v254, s5, 5
	v_writelane_b32 v254, s6, 6
	v_writelane_b32 v254, s7, 7
	v_writelane_b32 v254, s8, 8
	v_writelane_b32 v254, s9, 9
	v_writelane_b32 v254, s10, 10
	v_writelane_b32 v254, s11, 11
	v_writelane_b32 v254, s2, 12
	s_nop 1
	v_writelane_b32 v254, s3, 13
	s_and_b32 s2, s80, 7
	s_cmp_lg_u32 s2, 0
	s_cbranch_scc0 .LBB0_42
	s_load_dwordx2 s[96:97], s[0:1], 0xb8
	v_cmp_gt_u32_e32 vcc, 4, v0
	s_and_saveexec_b64 s[4:5], vcc

.LBB0_1232:
	s_add_u32 s58, s2, 0xffffff00
	s_addc_u32 s59, s49, -1
	s_lshl_b32 s2, s43, 2
	s_add_i32 s2, s2, 0
	s_add_i32 s2, s2, 0x24080
	v_mov_b32_e32 v42, v131
	v_mov_b32_e32 v43, s2
	ds_read_b32 v43, v43
	v_mbcnt_lo_u32_b32 v42, -1, v42
	s_lshl_b32 s2, s69, 8
	v_mbcnt_hi_u32_b32 v42, -1, v42
	s_add_i32 s2, s2, s78
	v_ashrrev_i32_e32 v44, 1, v42
	v_and_or_b32 v42, v42, 15, s2
	s_lshl_b32 s34, s26, 7
	s_waitcnt lgkmcnt(0)
	v_add_u32_e32 v136, v42, v43
	v_and_b32_e32 v44, -8, v44
	s_or_b32 s34, s34, s5
	v_add_u32_e32 v134, s34, v44
	v_ashrrev_i32_e32 v137, 31, v136
	v_ashrrev_i32_e32 v135, 31, v134
	s_mov_b64 s[34:35], 0x8000
	s_and_b64 vcc, exec, s[8:9]
	v_lshlrev_b64 v[44:45], 11, v[136:137]
	v_lshl_add_u64 v[44:45], s[16:17], 0, v[44:45]
	v_lshl_add_u64 v[134:135], v[44:45], 0, v[134:135]
	v_mov_b32_e32 v50, 0x43800000
	v_mov_b32_e32 v51, 0x43800000
	v_min_f32_e32 v94, 0x44e00000, v94
	v_min_f32_e32 v95, 0x44e00000, v95
	v_min_f32_e32 v96, 0x44e00000, v96
	v_min_f32_e32 v97, 0x44e00000, v97
	v_pk_mul_f32 v[46:47], v[94:95], s[100:101] op_sel_hi:[1,0]
	v_pk_mul_f32 v[48:49], v[96:97], s[100:101] op_sel_hi:[1,0]
	v_exp_f32_e32 v46, v46
	v_exp_f32_e32 v47, v47
	v_exp_f32_e32 v48, v48
	v_exp_f32_e32 v49, v49
	v_med3_f32 v62, v62, s82, v139
	v_med3_f32 v63, v63, s82, v139
	v_med3_f32 v64, v64, s82, v139
	v_med3_f32 v65, v65, s82, v139
	v_pk_add_f32 v[62:63], v[62:63], v[50:51]
	v_pk_add_f32 v[64:65], v[64:65], v[50:51]
	v_pk_add_f32 v[46:47], v[46:47], 1.0 op_sel_hi:[1,0]
	v_pk_add_f32 v[48:49], v[48:49], 1.0 op_sel_hi:[1,0]
	v_rcp_f32_e32 v46, v46
	v_rcp_f32_e32 v47, v47
	v_rcp_f32_e32 v48, v48
	v_rcp_f32_e32 v49, v49
	v_pk_mul_f32 v[94:95], v[94:95], s[100:101] op_sel:[0,1]
	v_pk_mul_f32 v[96:97], v[96:97], s[100:101] op_sel:[0,1]
	v_pk_mul_f32 v[94:95], v[94:95], v[46:47]
	v_pk_mul_f32 v[96:97], v[96:97], v[48:49]
	v_pk_mul_f32 v[94:95], v[94:95], v[62:63]
	v_pk_mul_f32 v[96:97], v[96:97], v[64:65]
	v_min_f32_e32 v90, 0x44e00000, v90
	v_min_f32_e32 v91, 0x44e00000, v91
	v_min_f32_e32 v92, 0x44e00000, v92
	v_min_f32_e32 v93, 0x44e00000, v93
	v_pk_mul_f32 v[46:47], v[90:91], s[100:101] op_sel_hi:[1,0]
	v_pk_mul_f32 v[48:49], v[92:93], s[100:101] op_sel_hi:[1,0]
	v_exp_f32_e32 v46, v46
	v_exp_f32_e32 v47, v47
	v_exp_f32_e32 v48, v48
	v_exp_f32_e32 v49, v49
	v_med3_f32 v58, v58, s82, v139
	v_med3_f32 v59, v59, s82, v139
	v_med3_f32 v60, v60, s82, v139
	v_med3_f32 v61, v61, s82, v139
	v_pk_add_f32 v[58:59], v[58:59], v[50:51]
	v_pk_add_f32 v[60:61], v[60:61], v[50:51]
	v_pk_add_f32 v[46:47], v[46:47], 1.0 op_sel_hi:[1,0]
	v_pk_add_f32 v[48:49], v[48:49], 1.0 op_sel_hi:[1,0]
	v_rcp_f32_e32 v46, v46
	v_rcp_f32_e32 v47, v47
	v_rcp_f32_e32 v48, v48
	v_rcp_f32_e32 v49, v49
	v_pk_mul_f32 v[90:91], v[90:91], s[100:101] op_sel:[0,1]
	v_pk_mul_f32 v[92:93], v[92:93], s[100:101] op_sel:[0,1]
	v_pk_mul_f32 v[90:91], v[90:91], v[46:47]
	v_pk_mul_f32 v[92:93], v[92:93], v[48:49]
	v_pk_mul_f32 v[90:91], v[90:91], v[58:59]
	v_pk_mul_f32 v[92:93], v[92:93], v[60:61]
	v_mov_b32_e32 v42, v131
	v_mov_b32_e32 v43, v131
	v_cvt_pk_fp8_f32 v42, v94, v95
	v_cvt_pk_fp8_f32 v43, v90, v91
	v_cvt_pk_fp8_f32 v42, v96, v97 op_sel:[0,0,1]
	v_cvt_pk_fp8_f32 v43, v92, v93 op_sel:[0,0,1]
	s_nop 0
	global_store_dwordx2 v[134:135], v[42:43], off sc1
	s_nop 1
	v_lshl_add_u64 v[44:45], v[134:135], 0, s[34:35]
	s_mov_b64 s[34:35], 0x10000
	v_min_f32_e32 v86, 0x44e00000, v86
	v_min_f32_e32 v87, 0x44e00000, v87
	v_min_f32_e32 v88, 0x44e00000, v88
	v_min_f32_e32 v89, 0x44e00000, v89
	v_pk_mul_f32 v[46:47], v[86:87], s[100:101] op_sel_hi:[1,0]
	v_pk_mul_f32 v[48:49], v[88:89], s[100:101] op_sel_hi:[1,0]
	v_exp_f32_e32 v46, v46
	v_exp_f32_e32 v47, v47
	v_exp_f32_e32 v48, v48
	v_exp_f32_e32 v49, v49
	v_med3_f32 v54, v54, s82, v139
	v_med3_f32 v55, v55, s82, v139
	v_med3_f32 v56, v56, s82, v139
	v_med3_f32 v57, v57, s82, v139
	v_pk_add_f32 v[54:55], v[54:55], v[50:51]
	v_pk_add_f32 v[56:57], v[56:57], v[50:51]
	v_pk_add_f32 v[46:47], v[46:47], 1.0 op_sel_hi:[1,0]
	v_pk_add_f32 v[48:49], v[48:49], 1.0 op_sel_hi:[1,0]
	v_rcp_f32_e32 v46, v46
	v_rcp_f32_e32 v47, v47
	v_rcp_f32_e32 v48, v48
	v_rcp_f32_e32 v49, v49
	v_pk_mul_f32 v[86:87], v[86:87], s[100:101] op_sel:[0,1]
	v_pk_mul_f32 v[88:89], v[88:89], s[100:101] op_sel:[0,1]
	v_pk_mul_f32 v[86:87], v[86:87], v[46:47]
	v_pk_mul_f32 v[88:89], v[88:89], v[48:49]
	v_pk_mul_f32 v[86:87], v[86:87], v[54:55]
	v_pk_mul_f32 v[88:89], v[88:89], v[56:57]
	v_min_f32_e32 v82, 0x44e00000, v82
	v_min_f32_e32 v83, 0x44e00000, v83
	v_min_f32_e32 v84, 0x44e00000, v84
	v_min_f32_e32 v85, 0x44e00000, v85
	v_pk_mul_f32 v[46:47], v[82:83], s[100:101] op_sel_hi:[1,0]
	v_pk_mul_f32 v[48:49], v[84:85], s[100:101] op_sel_hi:[1,0]
	v_exp_f32_e32 v46, v46
	v_exp_f32_e32 v47, v47
	v_exp_f32_e32 v48, v48
	v_exp_f32_e32 v49, v49
	v_med3_f32 v176, v176, s82, v139
	v_med3_f32 v177, v177, s82, v139
	v_med3_f32 v178, v178, s82, v139
	v_med3_f32 v179, v179, s82, v139
	v_pk_add_f32 v[176:177], v[176:177], v[50:51]
	v_pk_add_f32 v[178:179], v[178:179], v[50:51]
	v_pk_add_f32 v[46:47], v[46:47], 1.0 op_sel_hi:[1,0]
	v_pk_add_f32 v[48:49], v[48:49], 1.0 op_sel_hi:[1,0]
	v_rcp_f32_e32 v46, v46
	v_rcp_f32_e32 v47, v47
	v_rcp_f32_e32 v48, v48
	v_rcp_f32_e32 v49, v49
	v_pk_mul_f32 v[82:83], v[82:83], s[100:101] op_sel:[0,1]
	v_pk_mul_f32 v[84:85], v[84:85], s[100:101] op_sel:[0,1]
	v_pk_mul_f32 v[82:83], v[82:83], v[46:47]
	v_pk_mul_f32 v[84:85], v[84:85], v[48:49]
	v_pk_mul_f32 v[82:83], v[82:83], v[176:177]
	v_pk_mul_f32 v[84:85], v[84:85], v[178:179]
	v_mov_b32_e32 v42, v131
	v_mov_b32_e32 v43, v131
	v_cvt_pk_fp8_f32 v42, v86, v87
	v_cvt_pk_fp8_f32 v43, v82, v83
	v_cvt_pk_fp8_f32 v42, v88, v89 op_sel:[0,0,1]
	v_cvt_pk_fp8_f32 v43, v84, v85 op_sel:[0,0,1]
	s_nop 0
	global_store_dwordx2 v[44:45], v[42:43], off sc1
	s_nop 1
	v_lshl_add_u64 v[44:45], v[134:135], 0, s[34:35]
	s_mov_b64 s[34:35], 0x18000
	v_min_f32_e32 v78, 0x44e00000, v78
	v_min_f32_e32 v79, 0x44e00000, v79
	v_min_f32_e32 v80, 0x44e00000, v80
	v_min_f32_e32 v81, 0x44e00000, v81
	v_pk_mul_f32 v[46:47], v[78:79], s[100:101] op_sel_hi:[1,0]
	v_pk_mul_f32 v[48:49], v[80:81], s[100:101] op_sel_hi:[1,0]
	v_exp_f32_e32 v46, v46
	v_exp_f32_e32 v47, v47
	v_exp_f32_e32 v48, v48
	v_exp_f32_e32 v49, v49
	v_med3_f32 v172, v172, s82, v139
	v_med3_f32 v173, v173, s82, v139
	v_med3_f32 v174, v174, s82, v139
	v_med3_f32 v175, v175, s82, v139
	v_pk_add_f32 v[172:173], v[172:173], v[50:51]
	v_pk_add_f32 v[174:175], v[174:175], v[50:51]
	v_pk_add_f32 v[46:47], v[46:47], 1.0 op_sel_hi:[1,0]
	v_pk_add_f32 v[48:49], v[48:49], 1.0 op_sel_hi:[1,0]
	v_rcp_f32_e32 v46, v46
	v_rcp_f32_e32 v47, v47
	v_rcp_f32_e32 v48, v48
	v_rcp_f32_e32 v49, v49
	v_pk_mul_f32 v[78:79], v[78:79], s[100:101] op_sel:[0,1]
	v_pk_mul_f32 v[80:81], v[80:81], s[100:101] op_sel:[0,1]
	v_pk_mul_f32 v[78:79], v[78:79], v[46:47]
	v_pk_mul_f32 v[80:81], v[80:81], v[48:49]
	v_pk_mul_f32 v[78:79], v[78:79], v[172:173]
	v_pk_mul_f32 v[80:81], v[80:81], v[174:175]
	v_min_f32_e32 v74, 0x44e00000, v74
	v_min_f32_e32 v75, 0x44e00000, v75
	v_min_f32_e32 v76, 0x44e00000, v76
	v_min_f32_e32 v77, 0x44e00000, v77
	v_pk_mul_f32 v[46:47], v[74:75], s[100:101] op_sel_hi:[1,0]
	v_pk_mul_f32 v[48:49], v[76:77], s[100:101] op_sel_hi:[1,0]
	v_exp_f32_e32 v46, v46
	v_exp_f32_e32 v47, v47
	v_exp_f32_e32 v48, v48
	v_exp_f32_e32 v49, v49
	v_med3_f32 v18, v18, s82, v139
	v_med3_f32 v19, v19, s82, v139
	v_med3_f32 v20, v20, s82, v139
	v_med3_f32 v21, v21, s82, v139
	v_pk_add_f32 v[18:19], v[18:19], v[50:51]
	v_pk_add_f32 v[20:21], v[20:21], v[50:51]
	v_pk_add_f32 v[46:47], v[46:47], 1.0 op_sel_hi:[1,0]
	v_pk_add_f32 v[48:49], v[48:49], 1.0 op_sel_hi:[1,0]
	v_rcp_f32_e32 v46, v46
	v_rcp_f32_e32 v47, v47
	v_rcp_f32_e32 v48, v48
	v_rcp_f32_e32 v49, v49
	v_pk_mul_f32 v[74:75], v[74:75], s[100:101] op_sel:[0,1]
	v_pk_mul_f32 v[76:77], v[76:77], s[100:101] op_sel:[0,1]
	v_pk_mul_f32 v[74:75], v[74:75], v[46:47]
	v_pk_mul_f32 v[76:77], v[76:77], v[48:49]
	v_pk_mul_f32 v[74:75], v[74:75], v[18:19]
	v_pk_mul_f32 v[76:77], v[76:77], v[20:21]
	v_mov_b32_e32 v42, v131
	v_mov_b32_e32 v43, v131
	v_cvt_pk_fp8_f32 v42, v78, v79
	v_cvt_pk_fp8_f32 v43, v74, v75
	v_cvt_pk_fp8_f32 v42, v80, v81 op_sel:[0,0,1]
	v_cvt_pk_fp8_f32 v43, v76, v77 op_sel:[0,0,1]
	s_nop 0
	global_store_dwordx2 v[44:45], v[42:43], off sc1
	s_nop 1
	v_lshl_add_u64 v[44:45], v[134:135], 0, s[34:35]
	s_mov_b64 s[34:35], 0x48000
	v_min_f32_e32 v70, 0x44e00000, v70
	v_min_f32_e32 v71, 0x44e00000, v71
	v_min_f32_e32 v72, 0x44e00000, v72
	v_min_f32_e32 v73, 0x44e00000, v73
	v_pk_mul_f32 v[46:47], v[70:71], s[100:101] op_sel_hi:[1,0]
	v_pk_mul_f32 v[48:49], v[72:73], s[100:101] op_sel_hi:[1,0]
	v_exp_f32_e32 v46, v46
	v_exp_f32_e32 v47, v47
	v_exp_f32_e32 v48, v48
	v_exp_f32_e32 v49, v49
	v_med3_f32 v6, v6, s82, v139
	v_med3_f32 v7, v7, s82, v139
	v_med3_f32 v8, v8, s82, v139
	v_med3_f32 v9, v9, s82, v139
	v_pk_add_f32 v[6:7], v[6:7], v[50:51]
	v_pk_add_f32 v[8:9], v[8:9], v[50:51]
	v_pk_add_f32 v[46:47], v[46:47], 1.0 op_sel_hi:[1,0]
	v_pk_add_f32 v[48:49], v[48:49], 1.0 op_sel_hi:[1,0]
	v_rcp_f32_e32 v46, v46
	v_rcp_f32_e32 v47, v47
	v_rcp_f32_e32 v48, v48
	v_rcp_f32_e32 v49, v49
	v_pk_mul_f32 v[70:71], v[70:71], s[100:101] op_sel:[0,1]
	v_pk_mul_f32 v[72:73], v[72:73], s[100:101] op_sel:[0,1]
	v_pk_mul_f32 v[70:71], v[70:71], v[46:47]
	v_pk_mul_f32 v[72:73], v[72:73], v[48:49]
	v_pk_mul_f32 v[70:71], v[70:71], v[6:7]
	v_pk_mul_f32 v[72:73], v[72:73], v[8:9]
	v_min_f32_e32 v66, 0x44e00000, v66
	v_min_f32_e32 v67, 0x44e00000, v67
	v_min_f32_e32 v68, 0x44e00000, v68
	v_min_f32_e32 v69, 0x44e00000, v69
	v_pk_mul_f32 v[46:47], v[66:67], s[100:101] op_sel_hi:[1,0]
	v_pk_mul_f32 v[48:49], v[68:69], s[100:101] op_sel_hi:[1,0]
	v_exp_f32_e32 v46, v46
	v_exp_f32_e32 v47, v47
	v_exp_f32_e32 v48, v48
	v_exp_f32_e32 v49, v49
	v_med3_f32 v14, v14, s82, v139
	v_med3_f32 v15, v15, s82, v139
	v_med3_f32 v16, v16, s82, v139
	v_med3_f32 v17, v17, s82, v139
	v_pk_add_f32 v[14:15], v[14:15], v[50:51]
	v_pk_add_f32 v[16:17], v[16:17], v[50:51]
	v_pk_add_f32 v[46:47], v[46:47], 1.0 op_sel_hi:[1,0]
	v_pk_add_f32 v[48:49], v[48:49], 1.0 op_sel_hi:[1,0]
	v_rcp_f32_e32 v46, v46
	v_rcp_f32_e32 v47, v47
	v_rcp_f32_e32 v48, v48
	v_rcp_f32_e32 v49, v49
	v_pk_mul_f32 v[66:67], v[66:67], s[100:101] op_sel:[0,1]
	v_pk_mul_f32 v[68:69], v[68:69], s[100:101] op_sel:[0,1]
	v_pk_mul_f32 v[66:67], v[66:67], v[46:47]
	v_pk_mul_f32 v[68:69], v[68:69], v[48:49]
	v_pk_mul_f32 v[66:67], v[66:67], v[14:15]
	v_pk_mul_f32 v[68:69], v[68:69], v[16:17]
	v_mov_b32_e32 v42, v131
	v_mov_b32_e32 v43, v131
	v_cvt_pk_fp8_f32 v42, v70, v71
	v_cvt_pk_fp8_f32 v43, v66, v67
	v_cvt_pk_fp8_f32 v42, v72, v73 op_sel:[0,0,1]
	v_cvt_pk_fp8_f32 v43, v68, v69 op_sel:[0,0,1]
	s_nop 0
	global_store_dwordx2 v[44:45], v[42:43], off sc1
	s_nop 1
	v_lshl_add_u64 v[44:45], v[134:135], 0, s[22:23]
	v_min_f32_e32 v38, 0x44e00000, v38
	v_min_f32_e32 v39, 0x44e00000, v39
	v_min_f32_e32 v40, 0x44e00000, v40
	v_min_f32_e32 v41, 0x44e00000, v41
	v_pk_mul_f32 v[46:47], v[38:39], s[100:101] op_sel_hi:[1,0]
	v_pk_mul_f32 v[48:49], v[40:41], s[100:101] op_sel_hi:[1,0]
	v_exp_f32_e32 v46, v46
	v_exp_f32_e32 v47, v47
	v_exp_f32_e32 v48, v48
	v_exp_f32_e32 v49, v49
	v_med3_f32 v98, v98, s82, v139
	v_med3_f32 v99, v99, s82, v139
	v_med3_f32 v100, v100, s82, v139
	v_med3_f32 v101, v101, s82, v139
	v_pk_add_f32 v[98:99], v[98:99], v[50:51]
	v_pk_add_f32 v[100:101], v[100:101], v[50:51]
	v_pk_add_f32 v[46:47], v[46:47], 1.0 op_sel_hi:[1,0]
	v_pk_add_f32 v[48:49], v[48:49], 1.0 op_sel_hi:[1,0]
	v_rcp_f32_e32 v46, v46
	v_rcp_f32_e32 v47, v47
	v_rcp_f32_e32 v48, v48
	v_rcp_f32_e32 v49, v49
	v_pk_mul_f32 v[38:39], v[38:39], s[100:101] op_sel:[0,1]
	v_pk_mul_f32 v[40:41], v[40:41], s[100:101] op_sel:[0,1]
	v_pk_mul_f32 v[38:39], v[38:39], v[46:47]
	v_pk_mul_f32 v[40:41], v[40:41], v[48:49]
	v_pk_mul_f32 v[38:39], v[38:39], v[98:99]
	v_pk_mul_f32 v[40:41], v[40:41], v[100:101]
	v_min_f32_e32 v34, 0x44e00000, v34
	v_min_f32_e32 v35, 0x44e00000, v35
	v_min_f32_e32 v36, 0x44e00000, v36
	v_min_f32_e32 v37, 0x44e00000, v37
	v_pk_mul_f32 v[46:47], v[34:35], s[100:101] op_sel_hi:[1,0]
	v_pk_mul_f32 v[48:49], v[36:37], s[100:101] op_sel_hi:[1,0]
	v_exp_f32_e32 v46, v46
	v_exp_f32_e32 v47, v47
	v_exp_f32_e32 v48, v48
	v_exp_f32_e32 v49, v49
	v_med3_f32 v102, v102, s82, v139
	v_med3_f32 v103, v103, s82, v139
	v_med3_f32 v104, v104, s82, v139
	v_med3_f32 v105, v105, s82, v139
	v_pk_add_f32 v[102:103], v[102:103], v[50:51]
	v_pk_add_f32 v[104:105], v[104:105], v[50:51]
	v_pk_add_f32 v[46:47], v[46:47], 1.0 op_sel_hi:[1,0]
	v_pk_add_f32 v[48:49], v[48:49], 1.0 op_sel_hi:[1,0]
	v_rcp_f32_e32 v46, v46
	v_rcp_f32_e32 v47, v47
	v_rcp_f32_e32 v48, v48
	v_rcp_f32_e32 v49, v49
	v_pk_mul_f32 v[34:35], v[34:35], s[100:101] op_sel:[0,1]
	v_pk_mul_f32 v[36:37], v[36:37], s[100:101] op_sel:[0,1]
	v_pk_mul_f32 v[34:35], v[34:35], v[46:47]
	v_pk_mul_f32 v[36:37], v[36:37], v[48:49]
	v_pk_mul_f32 v[34:35], v[34:35], v[102:103]
	v_pk_mul_f32 v[36:37], v[36:37], v[104:105]
	v_mov_b32_e32 v42, v131
	v_mov_b32_e32 v43, v131
	v_cvt_pk_fp8_f32 v42, v38, v39
	v_cvt_pk_fp8_f32 v43, v34, v35
	v_cvt_pk_fp8_f32 v42, v40, v41 op_sel:[0,0,1]
	v_cvt_pk_fp8_f32 v43, v36, v37 op_sel:[0,0,1]
	s_nop 0
	global_store_dwordx2 v[44:45], v[42:43], off sc1
	s_nop 1
	v_lshl_add_u64 v[44:45], v[134:135], 0, s[34:35]
	s_mov_b64 s[34:35], 0x50000
	v_min_f32_e32 v30, 0x44e00000, v30
	v_min_f32_e32 v31, 0x44e00000, v31
	v_min_f32_e32 v32, 0x44e00000, v32
	v_min_f32_e32 v33, 0x44e00000, v33
	v_pk_mul_f32 v[46:47], v[30:31], s[100:101] op_sel_hi:[1,0]
	v_pk_mul_f32 v[48:49], v[32:33], s[100:101] op_sel_hi:[1,0]
	v_exp_f32_e32 v46, v46
	v_exp_f32_e32 v47, v47
	v_exp_f32_e32 v48, v48
	v_exp_f32_e32 v49, v49
	v_med3_f32 v106, v106, s82, v139
	v_med3_f32 v107, v107, s82, v139
	v_med3_f32 v108, v108, s82, v139
	v_med3_f32 v109, v109, s82, v139
	v_pk_add_f32 v[106:107], v[106:107], v[50:51]
	v_pk_add_f32 v[108:109], v[108:109], v[50:51]
	v_pk_add_f32 v[46:47], v[46:47], 1.0 op_sel_hi:[1,0]
	v_pk_add_f32 v[48:49], v[48:49], 1.0 op_sel_hi:[1,0]
	v_rcp_f32_e32 v46, v46
	v_rcp_f32_e32 v47, v47
	v_rcp_f32_e32 v48, v48
	v_rcp_f32_e32 v49, v49
	v_pk_mul_f32 v[30:31], v[30:31], s[100:101] op_sel:[0,1]
	v_pk_mul_f32 v[32:33], v[32:33], s[100:101] op_sel:[0,1]
	v_pk_mul_f32 v[30:31], v[30:31], v[46:47]
	v_pk_mul_f32 v[32:33], v[32:33], v[48:49]
	v_pk_mul_f32 v[30:31], v[30:31], v[106:107]
	v_pk_mul_f32 v[32:33], v[32:33], v[108:109]
	v_min_f32_e32 v26, 0x44e00000, v26
	v_min_f32_e32 v27, 0x44e00000, v27
	v_min_f32_e32 v28, 0x44e00000, v28
	v_min_f32_e32 v29, 0x44e00000, v29
	v_pk_mul_f32 v[46:47], v[26:27], s[100:101] op_sel_hi:[1,0]
	v_pk_mul_f32 v[48:49], v[28:29], s[100:101] op_sel_hi:[1,0]
	v_exp_f32_e32 v46, v46
	v_exp_f32_e32 v47, v47
	v_exp_f32_e32 v48, v48
	v_exp_f32_e32 v49, v49
	v_med3_f32 v110, v110, s82, v139
	v_med3_f32 v111, v111, s82, v139
	v_med3_f32 v112, v112, s82, v139
	v_med3_f32 v113, v113, s82, v139
	v_pk_add_f32 v[110:111], v[110:111], v[50:51]
	v_pk_add_f32 v[112:113], v[112:113], v[50:51]
	v_pk_add_f32 v[46:47], v[46:47], 1.0 op_sel_hi:[1,0]
	v_pk_add_f32 v[48:49], v[48:49], 1.0 op_sel_hi:[1,0]
	v_rcp_f32_e32 v46, v46
	v_rcp_f32_e32 v47, v47
	v_rcp_f32_e32 v48, v48
	v_rcp_f32_e32 v49, v49
	v_pk_mul_f32 v[26:27], v[26:27], s[100:101] op_sel:[0,1]
	v_pk_mul_f32 v[28:29], v[28:29], s[100:101] op_sel:[0,1]
	v_pk_mul_f32 v[26:27], v[26:27], v[46:47]
	v_pk_mul_f32 v[28:29], v[28:29], v[48:49]
	v_pk_mul_f32 v[26:27], v[26:27], v[110:111]
	v_pk_mul_f32 v[28:29], v[28:29], v[112:113]
	v_mov_b32_e32 v42, v131
	v_mov_b32_e32 v43, v131
	v_cvt_pk_fp8_f32 v42, v30, v31
	v_cvt_pk_fp8_f32 v43, v26, v27
	v_cvt_pk_fp8_f32 v42, v32, v33 op_sel:[0,0,1]
	v_cvt_pk_fp8_f32 v43, v28, v29 op_sel:[0,0,1]
	s_nop 0
	global_store_dwordx2 v[44:45], v[42:43], off sc1
	s_nop 1
	v_lshl_add_u64 v[44:45], v[134:135], 0, s[34:35]
	s_mov_b64 s[34:35], 0x58000
	v_min_f32_e32 v22, 0x44e00000, v22
	v_min_f32_e32 v23, 0x44e00000, v23
	v_min_f32_e32 v24, 0x44e00000, v24
	v_min_f32_e32 v25, 0x44e00000, v25
	v_pk_mul_f32 v[46:47], v[22:23], s[100:101] op_sel_hi:[1,0]
	v_pk_mul_f32 v[48:49], v[24:25], s[100:101] op_sel_hi:[1,0]
	v_exp_f32_e32 v46, v46
	v_exp_f32_e32 v47, v47
	v_exp_f32_e32 v48, v48
	v_exp_f32_e32 v49, v49
	v_med3_f32 v114, v114, s82, v139
	v_med3_f32 v115, v115, s82, v139
	v_med3_f32 v116, v116, s82, v139
	v_med3_f32 v117, v117, s82, v139
	v_pk_add_f32 v[114:115], v[114:115], v[50:51]
	v_pk_add_f32 v[116:117], v[116:117], v[50:51]
	v_pk_add_f32 v[46:47], v[46:47], 1.0 op_sel_hi:[1,0]
	v_pk_add_f32 v[48:49], v[48:49], 1.0 op_sel_hi:[1,0]
	v_rcp_f32_e32 v46, v46
	v_rcp_f32_e32 v47, v47
	v_rcp_f32_e32 v48, v48
	v_rcp_f32_e32 v49, v49
	v_pk_mul_f32 v[22:23], v[22:23], s[100:101] op_sel:[0,1]
	v_pk_mul_f32 v[24:25], v[24:25], s[100:101] op_sel:[0,1]
	v_pk_mul_f32 v[22:23], v[22:23], v[46:47]
	v_pk_mul_f32 v[24:25], v[24:25], v[48:49]
	v_pk_mul_f32 v[22:23], v[22:23], v[114:115]
	v_pk_mul_f32 v[24:25], v[24:25], v[116:117]
	v_min_f32_e32 v220, 0x44e00000, v220
	v_min_f32_e32 v221, 0x44e00000, v221
	v_min_f32_e32 v222, 0x44e00000, v222
	v_min_f32_e32 v223, 0x44e00000, v223
	v_pk_mul_f32 v[46:47], v[220:221], s[100:101] op_sel_hi:[1,0]
	v_pk_mul_f32 v[48:49], v[222:223], s[100:101] op_sel_hi:[1,0]
	v_exp_f32_e32 v46, v46
	v_exp_f32_e32 v47, v47
	v_exp_f32_e32 v48, v48
	v_exp_f32_e32 v49, v49
	v_med3_f32 v118, v118, s82, v139
	v_med3_f32 v119, v119, s82, v139
	v_med3_f32 v120, v120, s82, v139
	v_med3_f32 v121, v121, s82, v139
	v_pk_add_f32 v[118:119], v[118:119], v[50:51]
	v_pk_add_f32 v[120:121], v[120:121], v[50:51]
	v_pk_add_f32 v[46:47], v[46:47], 1.0 op_sel_hi:[1,0]
	v_pk_add_f32 v[48:49], v[48:49], 1.0 op_sel_hi:[1,0]
	v_rcp_f32_e32 v46, v46
	v_rcp_f32_e32 v47, v47
	v_rcp_f32_e32 v48, v48
	v_rcp_f32_e32 v49, v49
	v_pk_mul_f32 v[220:221], v[220:221], s[100:101] op_sel:[0,1]
	v_pk_mul_f32 v[222:223], v[222:223], s[100:101] op_sel:[0,1]
	v_pk_mul_f32 v[220:221], v[220:221], v[46:47]
	v_pk_mul_f32 v[222:223], v[222:223], v[48:49]
	v_pk_mul_f32 v[220:221], v[220:221], v[118:119]
	v_pk_mul_f32 v[222:223], v[222:223], v[120:121]
	v_mov_b32_e32 v42, v131
	v_mov_b32_e32 v43, v131
	v_cvt_pk_fp8_f32 v42, v22, v23
	v_cvt_pk_fp8_f32 v43, v220, v221
	v_cvt_pk_fp8_f32 v42, v24, v25 op_sel:[0,0,1]
	v_cvt_pk_fp8_f32 v43, v222, v223 op_sel:[0,0,1]
	s_nop 0
	global_store_dwordx2 v[44:45], v[42:43], off sc1
	s_nop 1
	v_lshl_add_u64 v[44:45], v[134:135], 0, s[34:35]
	v_min_f32_e32 v2, 0x44e00000, v2
	v_min_f32_e32 v3, 0x44e00000, v3
	v_min_f32_e32 v4, 0x44e00000, v4
	v_min_f32_e32 v5, 0x44e00000, v5
	v_pk_mul_f32 v[46:47], v[2:3], s[100:101] op_sel_hi:[1,0]
	v_pk_mul_f32 v[48:49], v[4:5], s[100:101] op_sel_hi:[1,0]
	v_exp_f32_e32 v46, v46
	v_exp_f32_e32 v47, v47
	v_exp_f32_e32 v48, v48
	v_exp_f32_e32 v49, v49
	v_med3_f32 v122, v122, s82, v139
	v_med3_f32 v123, v123, s82, v139
	v_med3_f32 v124, v124, s82, v139
	v_med3_f32 v125, v125, s82, v139
	v_pk_add_f32 v[122:123], v[122:123], v[50:51]
	v_pk_add_f32 v[124:125], v[124:125], v[50:51]
	v_pk_add_f32 v[46:47], v[46:47], 1.0 op_sel_hi:[1,0]
	v_pk_add_f32 v[48:49], v[48:49], 1.0 op_sel_hi:[1,0]
	v_rcp_f32_e32 v46, v46
	v_rcp_f32_e32 v47, v47
	v_rcp_f32_e32 v48, v48
	v_rcp_f32_e32 v49, v49
	v_pk_mul_f32 v[2:3], v[2:3], s[100:101] op_sel:[0,1]
	v_pk_mul_f32 v[4:5], v[4:5], s[100:101] op_sel:[0,1]
	v_pk_mul_f32 v[2:3], v[2:3], v[46:47]
	v_pk_mul_f32 v[4:5], v[4:5], v[48:49]
	v_pk_mul_f32 v[2:3], v[2:3], v[122:123]
	v_pk_mul_f32 v[4:5], v[4:5], v[124:125]
	v_min_f32_e32 v10, 0x44e00000, v10
	v_min_f32_e32 v11, 0x44e00000, v11
	v_min_f32_e32 v12, 0x44e00000, v12
	v_min_f32_e32 v13, 0x44e00000, v13
	v_pk_mul_f32 v[46:47], v[10:11], s[100:101] op_sel_hi:[1,0]
	v_pk_mul_f32 v[48:49], v[12:13], s[100:101] op_sel_hi:[1,0]
	v_exp_f32_e32 v46, v46
	v_exp_f32_e32 v47, v47
	v_exp_f32_e32 v48, v48
	v_exp_f32_e32 v49, v49
	v_med3_f32 v126, v126, s82, v139
	v_med3_f32 v127, v127, s82, v139
	v_med3_f32 v128, v128, s82, v139
	v_med3_f32 v129, v129, s82, v139
	v_pk_add_f32 v[126:127], v[126:127], v[50:51]
	v_pk_add_f32 v[128:129], v[128:129], v[50:51]
	v_pk_add_f32 v[46:47], v[46:47], 1.0 op_sel_hi:[1,0]
	v_pk_add_f32 v[48:49], v[48:49], 1.0 op_sel_hi:[1,0]
	v_rcp_f32_e32 v46, v46
	v_rcp_f32_e32 v47, v47
	v_rcp_f32_e32 v48, v48
	v_rcp_f32_e32 v49, v49
	v_pk_mul_f32 v[10:11], v[10:11], s[100:101] op_sel:[0,1]
	v_pk_mul_f32 v[12:13], v[12:13], s[100:101] op_sel:[0,1]
	v_pk_mul_f32 v[10:11], v[10:11], v[46:47]
	v_pk_mul_f32 v[12:13], v[12:13], v[48:49]
	v_pk_mul_f32 v[10:11], v[10:11], v[126:127]
	v_pk_mul_f32 v[12:13], v[12:13], v[128:129]
	v_mov_b32_e32 v42, v131
	v_mov_b32_e32 v43, v131
	v_cvt_pk_fp8_f32 v42, v2, v3
	v_cvt_pk_fp8_f32 v43, v10, v11
	v_cvt_pk_fp8_f32 v42, v4, v5 op_sel:[0,0,1]
	v_cvt_pk_fp8_f32 v43, v12, v13 op_sel:[0,0,1]
	s_nop 0
	global_store_dwordx2 v[44:45], v[42:43], off sc1
	s_nop 1
	s_cbranch_vccnz .LBB0_1236
	s_ashr_i32 s49, s48, 31
	v_readlane_b32 s88, v254, 4
	s_lshl_b64 s[8:9], s[48:49], 14
	v_readlane_b32 s92, v254, 8
	v_readlane_b32 s93, v254, 9
	s_add_u32 s2, s92, s8
	v_mov_b32_e32 v2, v131
	s_addc_u32 s26, s93, s9
	s_lshl_b32 s8, s50, 7
	s_ashr_i32 s9, s8, 31
	v_mbcnt_lo_u32_b32 v2, -1, v2
	s_lshl_b64 s[8:9], s[8:9], 2
	v_mbcnt_hi_u32_b32 v2, -1, v2
	s_add_u32 s2, s2, s8
	s_addc_u32 s9, s26, s9
	s_lshl_b32 s8, s5, 2
	v_ashrrev_i32_e32 v2, 1, v2
	s_add_u32 s8, s2, s8
	v_and_b32_e32 v2, -8, v2
	s_addc_u32 s9, s9, 0
	v_ashrrev_i32_e32 v3, 31, v2
	v_lshl_add_u64 v[6:7], v[2:3], 2, s[8:9]
	v_lshl_add_u64 v[14:15], v[6:7], 0, s[18:19]
	global_load_dwordx4 v[10:13], v[6:7], off offset:16
	global_load_dwordx4 v[2:5], v[6:7], off
	v_add_co_u32_e32 v6, vcc, 0x2000, v6
	v_readlane_b32 s89, v254, 5
	s_nop 0
	v_addc_co_u32_e32 v7, vcc, 0, v7, vcc
	global_load_dwordx4 v[6:9], v[6:7], off
	s_nop 0
	global_load_dwordx4 v[14:17], v[14:15], off offset:16
	s_andn2_b64 vcc, exec, s[28:29]
	v_readlane_b32 s90, v254, 6
	v_readlane_b32 s91, v254, 7
	v_readlane_b32 s94, v254, 10
	v_readlane_b32 s95, v254, 11
	s_cbranch_vccnz .LBB0_1235
	s_barrier

.LBB0_1265:
	s_add_u32 s54, s45, 0xffffff00
	s_addc_u32 s55, s47, -1
	s_lshl_b32 s34, s64, 2
	s_add_i32 s34, s34, 0
	s_add_i32 s34, s34, 0x24080
	v_mov_b32_e32 v42, v131
	v_mov_b32_e32 v43, s34
	ds_read_b32 v43, v43
	v_mbcnt_lo_u32_b32 v42, -1, v42
	s_lshl_b32 s34, s65, 8
	v_mbcnt_hi_u32_b32 v42, -1, v42
	s_add_i32 s34, s34, s77
	v_ashrrev_i32_e32 v44, 1, v42
	v_and_or_b32 v42, v42, 15, s34
	s_lshl_b32 s35, s22, 7
	s_waitcnt lgkmcnt(0)
	v_add_u32_e32 v136, v42, v43
	v_and_b32_e32 v44, -8, v44
	s_or_b32 s35, s35, s63
	v_add_u32_e32 v134, s35, v44
	v_ashrrev_i32_e32 v137, 31, v136
	v_ashrrev_i32_e32 v135, 31, v134
	s_mov_b64 s[34:35], 0x8000
	s_and_b64 vcc, exec, s[4:5]
	v_lshlrev_b64 v[44:45], 11, v[136:137]
	v_lshl_add_u64 v[44:45], s[16:17], 0, v[44:45]
	v_lshl_add_u64 v[134:135], v[44:45], 0, v[134:135]
	v_mov_b32_e32 v50, 0x43800000
	v_mov_b32_e32 v51, 0x43800000
	v_min_f32_e32 v94, 0x44e00000, v94
	v_min_f32_e32 v95, 0x44e00000, v95
	v_min_f32_e32 v96, 0x44e00000, v96
	v_min_f32_e32 v97, 0x44e00000, v97
	v_pk_mul_f32 v[46:47], v[94:95], s[100:101] op_sel_hi:[1,0]
	v_pk_mul_f32 v[48:49], v[96:97], s[100:101] op_sel_hi:[1,0]
	v_exp_f32_e32 v46, v46
	v_exp_f32_e32 v47, v47
	v_exp_f32_e32 v48, v48
	v_exp_f32_e32 v49, v49
	v_med3_f32 v62, v62, s81, v139
	v_med3_f32 v63, v63, s81, v139
	v_med3_f32 v64, v64, s81, v139
	v_med3_f32 v65, v65, s81, v139
	v_pk_add_f32 v[62:63], v[62:63], v[50:51]
	v_pk_add_f32 v[64:65], v[64:65], v[50:51]
	v_pk_add_f32 v[46:47], v[46:47], 1.0 op_sel_hi:[1,0]
	v_pk_add_f32 v[48:49], v[48:49], 1.0 op_sel_hi:[1,0]
	v_rcp_f32_e32 v46, v46
	v_rcp_f32_e32 v47, v47
	v_rcp_f32_e32 v48, v48
	v_rcp_f32_e32 v49, v49
	v_pk_mul_f32 v[94:95], v[94:95], s[100:101] op_sel:[0,1]
	v_pk_mul_f32 v[96:97], v[96:97], s[100:101] op_sel:[0,1]
	v_pk_mul_f32 v[94:95], v[94:95], v[46:47]
	v_pk_mul_f32 v[96:97], v[96:97], v[48:49]
	v_pk_mul_f32 v[94:95], v[94:95], v[62:63]
	v_pk_mul_f32 v[96:97], v[96:97], v[64:65]
	v_min_f32_e32 v90, 0x44e00000, v90
	v_min_f32_e32 v91, 0x44e00000, v91
	v_min_f32_e32 v92, 0x44e00000, v92
	v_min_f32_e32 v93, 0x44e00000, v93
	v_pk_mul_f32 v[46:47], v[90:91], s[100:101] op_sel_hi:[1,0]
	v_pk_mul_f32 v[48:49], v[92:93], s[100:101] op_sel_hi:[1,0]
	v_exp_f32_e32 v46, v46
	v_exp_f32_e32 v47, v47
	v_exp_f32_e32 v48, v48
	v_exp_f32_e32 v49, v49
	v_med3_f32 v58, v58, s81, v139
	v_med3_f32 v59, v59, s81, v139
	v_med3_f32 v60, v60, s81, v139
	v_med3_f32 v61, v61, s81, v139
	v_pk_add_f32 v[58:59], v[58:59], v[50:51]
	v_pk_add_f32 v[60:61], v[60:61], v[50:51]
	v_pk_add_f32 v[46:47], v[46:47], 1.0 op_sel_hi:[1,0]
	v_pk_add_f32 v[48:49], v[48:49], 1.0 op_sel_hi:[1,0]
	v_rcp_f32_e32 v46, v46
	v_rcp_f32_e32 v47, v47
	v_rcp_f32_e32 v48, v48
	v_rcp_f32_e32 v49, v49
	v_pk_mul_f32 v[90:91], v[90:91], s[100:101] op_sel:[0,1]
	v_pk_mul_f32 v[92:93], v[92:93], s[100:101] op_sel:[0,1]
	v_pk_mul_f32 v[90:91], v[90:91], v[46:47]
	v_pk_mul_f32 v[92:93], v[92:93], v[48:49]
	v_pk_mul_f32 v[90:91], v[90:91], v[58:59]
	v_pk_mul_f32 v[92:93], v[92:93], v[60:61]
	v_mov_b32_e32 v42, v131
	v_mov_b32_e32 v43, v131
	v_cvt_pk_fp8_f32 v42, v94, v95
	v_cvt_pk_fp8_f32 v43, v90, v91
	v_cvt_pk_fp8_f32 v42, v96, v97 op_sel:[0,0,1]
	v_cvt_pk_fp8_f32 v43, v92, v93 op_sel:[0,0,1]
	s_nop 0
	global_store_dwordx2 v[134:135], v[42:43], off sc1
	s_nop 1
	v_lshl_add_u64 v[44:45], v[134:135], 0, s[34:35]
	s_mov_b64 s[34:35], 0x10000
	v_min_f32_e32 v86, 0x44e00000, v86
	v_min_f32_e32 v87, 0x44e00000, v87
	v_min_f32_e32 v88, 0x44e00000, v88
	v_min_f32_e32 v89, 0x44e00000, v89
	v_pk_mul_f32 v[46:47], v[86:87], s[100:101] op_sel_hi:[1,0]
	v_pk_mul_f32 v[48:49], v[88:89], s[100:101] op_sel_hi:[1,0]
	v_exp_f32_e32 v46, v46
	v_exp_f32_e32 v47, v47
	v_exp_f32_e32 v48, v48
	v_exp_f32_e32 v49, v49
	v_med3_f32 v54, v54, s81, v139
	v_med3_f32 v55, v55, s81, v139
	v_med3_f32 v56, v56, s81, v139
	v_med3_f32 v57, v57, s81, v139
	v_pk_add_f32 v[54:55], v[54:55], v[50:51]
	v_pk_add_f32 v[56:57], v[56:57], v[50:51]
	v_pk_add_f32 v[46:47], v[46:47], 1.0 op_sel_hi:[1,0]
	v_pk_add_f32 v[48:49], v[48:49], 1.0 op_sel_hi:[1,0]
	v_rcp_f32_e32 v46, v46
	v_rcp_f32_e32 v47, v47
	v_rcp_f32_e32 v48, v48
	v_rcp_f32_e32 v49, v49
	v_pk_mul_f32 v[86:87], v[86:87], s[100:101] op_sel:[0,1]
	v_pk_mul_f32 v[88:89], v[88:89], s[100:101] op_sel:[0,1]
	v_pk_mul_f32 v[86:87], v[86:87], v[46:47]
	v_pk_mul_f32 v[88:89], v[88:89], v[48:49]
	v_pk_mul_f32 v[86:87], v[86:87], v[54:55]
	v_pk_mul_f32 v[88:89], v[88:89], v[56:57]
	v_min_f32_e32 v82, 0x44e00000, v82
	v_min_f32_e32 v83, 0x44e00000, v83
	v_min_f32_e32 v84, 0x44e00000, v84
	v_min_f32_e32 v85, 0x44e00000, v85
	v_pk_mul_f32 v[46:47], v[82:83], s[100:101] op_sel_hi:[1,0]
	v_pk_mul_f32 v[48:49], v[84:85], s[100:101] op_sel_hi:[1,0]
	v_exp_f32_e32 v46, v46
	v_exp_f32_e32 v47, v47
	v_exp_f32_e32 v48, v48
	v_exp_f32_e32 v49, v49
	v_med3_f32 v176, v176, s81, v139
	v_med3_f32 v177, v177, s81, v139
	v_med3_f32 v178, v178, s81, v139
	v_med3_f32 v179, v179, s81, v139
	v_pk_add_f32 v[176:177], v[176:177], v[50:51]
	v_pk_add_f32 v[178:179], v[178:179], v[50:51]
	v_pk_add_f32 v[46:47], v[46:47], 1.0 op_sel_hi:[1,0]
	v_pk_add_f32 v[48:49], v[48:49], 1.0 op_sel_hi:[1,0]
	v_rcp_f32_e32 v46, v46
	v_rcp_f32_e32 v47, v47
	v_rcp_f32_e32 v48, v48
	v_rcp_f32_e32 v49, v49
	v_pk_mul_f32 v[82:83], v[82:83], s[100:101] op_sel:[0,1]
	v_pk_mul_f32 v[84:85], v[84:85], s[100:101] op_sel:[0,1]
	v_pk_mul_f32 v[82:83], v[82:83], v[46:47]
	v_pk_mul_f32 v[84:85], v[84:85], v[48:49]
	v_pk_mul_f32 v[82:83], v[82:83], v[176:177]
	v_pk_mul_f32 v[84:85], v[84:85], v[178:179]
	v_mov_b32_e32 v42, v131
	v_mov_b32_e32 v43, v131
	v_cvt_pk_fp8_f32 v42, v86, v87
	v_cvt_pk_fp8_f32 v43, v82, v83
	v_cvt_pk_fp8_f32 v42, v88, v89 op_sel:[0,0,1]
	v_cvt_pk_fp8_f32 v43, v84, v85 op_sel:[0,0,1]
	s_nop 0
	global_store_dwordx2 v[44:45], v[42:43], off sc1
	s_nop 1
	v_lshl_add_u64 v[44:45], v[134:135], 0, s[34:35]
	s_mov_b64 s[34:35], 0x18000
	v_min_f32_e32 v78, 0x44e00000, v78
	v_min_f32_e32 v79, 0x44e00000, v79
	v_min_f32_e32 v80, 0x44e00000, v80
	v_min_f32_e32 v81, 0x44e00000, v81
	v_pk_mul_f32 v[46:47], v[78:79], s[100:101] op_sel_hi:[1,0]
	v_pk_mul_f32 v[48:49], v[80:81], s[100:101] op_sel_hi:[1,0]
	v_exp_f32_e32 v46, v46
	v_exp_f32_e32 v47, v47
	v_exp_f32_e32 v48, v48
	v_exp_f32_e32 v49, v49
	v_med3_f32 v172, v172, s81, v139
	v_med3_f32 v173, v173, s81, v139
	v_med3_f32 v174, v174, s81, v139
	v_med3_f32 v175, v175, s81, v139
	v_pk_add_f32 v[172:173], v[172:173], v[50:51]
	v_pk_add_f32 v[174:175], v[174:175], v[50:51]
	v_pk_add_f32 v[46:47], v[46:47], 1.0 op_sel_hi:[1,0]
	v_pk_add_f32 v[48:49], v[48:49], 1.0 op_sel_hi:[1,0]
	v_rcp_f32_e32 v46, v46
	v_rcp_f32_e32 v47, v47
	v_rcp_f32_e32 v48, v48
	v_rcp_f32_e32 v49, v49
	v_pk_mul_f32 v[78:79], v[78:79], s[100:101] op_sel:[0,1]
	v_pk_mul_f32 v[80:81], v[80:81], s[100:101] op_sel:[0,1]
	v_pk_mul_f32 v[78:79], v[78:79], v[46:47]
	v_pk_mul_f32 v[80:81], v[80:81], v[48:49]
	v_pk_mul_f32 v[78:79], v[78:79], v[172:173]
	v_pk_mul_f32 v[80:81], v[80:81], v[174:175]
	v_min_f32_e32 v74, 0x44e00000, v74
	v_min_f32_e32 v75, 0x44e00000, v75
	v_min_f32_e32 v76, 0x44e00000, v76
	v_min_f32_e32 v77, 0x44e00000, v77
	v_pk_mul_f32 v[46:47], v[74:75], s[100:101] op_sel_hi:[1,0]
	v_pk_mul_f32 v[48:49], v[76:77], s[100:101] op_sel_hi:[1,0]
	v_exp_f32_e32 v46, v46
	v_exp_f32_e32 v47, v47
	v_exp_f32_e32 v48, v48
	v_exp_f32_e32 v49, v49
	v_med3_f32 v18, v18, s81, v139
	v_med3_f32 v19, v19, s81, v139
	v_med3_f32 v20, v20, s81, v139
	v_med3_f32 v21, v21, s81, v139
	v_pk_add_f32 v[18:19], v[18:19], v[50:51]
	v_pk_add_f32 v[20:21], v[20:21], v[50:51]
	v_pk_add_f32 v[46:47], v[46:47], 1.0 op_sel_hi:[1,0]
	v_pk_add_f32 v[48:49], v[48:49], 1.0 op_sel_hi:[1,0]
	v_rcp_f32_e32 v46, v46
	v_rcp_f32_e32 v47, v47
	v_rcp_f32_e32 v48, v48
	v_rcp_f32_e32 v49, v49
	v_pk_mul_f32 v[74:75], v[74:75], s[100:101] op_sel:[0,1]
	v_pk_mul_f32 v[76:77], v[76:77], s[100:101] op_sel:[0,1]
	v_pk_mul_f32 v[74:75], v[74:75], v[46:47]
	v_pk_mul_f32 v[76:77], v[76:77], v[48:49]
	v_pk_mul_f32 v[74:75], v[74:75], v[18:19]
	v_pk_mul_f32 v[76:77], v[76:77], v[20:21]
	v_mov_b32_e32 v42, v131
	v_mov_b32_e32 v43, v131
	v_cvt_pk_fp8_f32 v42, v78, v79
	v_cvt_pk_fp8_f32 v43, v74, v75
	v_cvt_pk_fp8_f32 v42, v80, v81 op_sel:[0,0,1]
	v_cvt_pk_fp8_f32 v43, v76, v77 op_sel:[0,0,1]
	s_nop 0
	global_store_dwordx2 v[44:45], v[42:43], off sc1
	s_nop 1
	v_lshl_add_u64 v[44:45], v[134:135], 0, s[34:35]
	s_mov_b64 s[34:35], 0x48000
	v_min_f32_e32 v70, 0x44e00000, v70
	v_min_f32_e32 v71, 0x44e00000, v71
	v_min_f32_e32 v72, 0x44e00000, v72
	v_min_f32_e32 v73, 0x44e00000, v73
	v_pk_mul_f32 v[46:47], v[70:71], s[100:101] op_sel_hi:[1,0]
	v_pk_mul_f32 v[48:49], v[72:73], s[100:101] op_sel_hi:[1,0]
	v_exp_f32_e32 v46, v46
	v_exp_f32_e32 v47, v47
	v_exp_f32_e32 v48, v48
	v_exp_f32_e32 v49, v49
	v_med3_f32 v6, v6, s81, v139
	v_med3_f32 v7, v7, s81, v139
	v_med3_f32 v8, v8, s81, v139
	v_med3_f32 v9, v9, s81, v139
	v_pk_add_f32 v[6:7], v[6:7], v[50:51]
	v_pk_add_f32 v[8:9], v[8:9], v[50:51]
	v_pk_add_f32 v[46:47], v[46:47], 1.0 op_sel_hi:[1,0]
	v_pk_add_f32 v[48:49], v[48:49], 1.0 op_sel_hi:[1,0]
	v_rcp_f32_e32 v46, v46
	v_rcp_f32_e32 v47, v47
	v_rcp_f32_e32 v48, v48
	v_rcp_f32_e32 v49, v49
	v_pk_mul_f32 v[70:71], v[70:71], s[100:101] op_sel:[0,1]
	v_pk_mul_f32 v[72:73], v[72:73], s[100:101] op_sel:[0,1]
	v_pk_mul_f32 v[70:71], v[70:71], v[46:47]
	v_pk_mul_f32 v[72:73], v[72:73], v[48:49]
	v_pk_mul_f32 v[70:71], v[70:71], v[6:7]
	v_pk_mul_f32 v[72:73], v[72:73], v[8:9]
	v_min_f32_e32 v66, 0x44e00000, v66
	v_min_f32_e32 v67, 0x44e00000, v67
	v_min_f32_e32 v68, 0x44e00000, v68
	v_min_f32_e32 v69, 0x44e00000, v69
	v_pk_mul_f32 v[46:47], v[66:67], s[100:101] op_sel_hi:[1,0]
	v_pk_mul_f32 v[48:49], v[68:69], s[100:101] op_sel_hi:[1,0]
	v_exp_f32_e32 v46, v46
	v_exp_f32_e32 v47, v47
	v_exp_f32_e32 v48, v48
	v_exp_f32_e32 v49, v49
	v_med3_f32 v14, v14, s81, v139
	v_med3_f32 v15, v15, s81, v139
	v_med3_f32 v16, v16, s81, v139
	v_med3_f32 v17, v17, s81, v139
	v_pk_add_f32 v[14:15], v[14:15], v[50:51]
	v_pk_add_f32 v[16:17], v[16:17], v[50:51]
	v_pk_add_f32 v[46:47], v[46:47], 1.0 op_sel_hi:[1,0]
	v_pk_add_f32 v[48:49], v[48:49], 1.0 op_sel_hi:[1,0]
	v_rcp_f32_e32 v46, v46
	v_rcp_f32_e32 v47, v47
	v_rcp_f32_e32 v48, v48
	v_rcp_f32_e32 v49, v49
	v_pk_mul_f32 v[66:67], v[66:67], s[100:101] op_sel:[0,1]
	v_pk_mul_f32 v[68:69], v[68:69], s[100:101] op_sel:[0,1]
	v_pk_mul_f32 v[66:67], v[66:67], v[46:47]
	v_pk_mul_f32 v[68:69], v[68:69], v[48:49]
	v_pk_mul_f32 v[66:67], v[66:67], v[14:15]
	v_pk_mul_f32 v[68:69], v[68:69], v[16:17]
	v_mov_b32_e32 v42, v131
	v_mov_b32_e32 v43, v131
	v_cvt_pk_fp8_f32 v42, v70, v71
	v_cvt_pk_fp8_f32 v43, v66, v67
	v_cvt_pk_fp8_f32 v42, v72, v73 op_sel:[0,0,1]
	v_cvt_pk_fp8_f32 v43, v68, v69 op_sel:[0,0,1]
	s_nop 0
	global_store_dwordx2 v[44:45], v[42:43], off sc1
	s_nop 1
	v_lshl_add_u64 v[44:45], v[134:135], 0, s[18:19]
	v_min_f32_e32 v38, 0x44e00000, v38
	v_min_f32_e32 v39, 0x44e00000, v39
	v_min_f32_e32 v40, 0x44e00000, v40
	v_min_f32_e32 v41, 0x44e00000, v41
	v_pk_mul_f32 v[46:47], v[38:39], s[100:101] op_sel_hi:[1,0]
	v_pk_mul_f32 v[48:49], v[40:41], s[100:101] op_sel_hi:[1,0]
	v_exp_f32_e32 v46, v46
	v_exp_f32_e32 v47, v47
	v_exp_f32_e32 v48, v48
	v_exp_f32_e32 v49, v49
	v_med3_f32 v98, v98, s81, v139
	v_med3_f32 v99, v99, s81, v139
	v_med3_f32 v100, v100, s81, v139
	v_med3_f32 v101, v101, s81, v139
	v_pk_add_f32 v[98:99], v[98:99], v[50:51]
	v_pk_add_f32 v[100:101], v[100:101], v[50:51]
	v_pk_add_f32 v[46:47], v[46:47], 1.0 op_sel_hi:[1,0]
	v_pk_add_f32 v[48:49], v[48:49], 1.0 op_sel_hi:[1,0]
	v_rcp_f32_e32 v46, v46
	v_rcp_f32_e32 v47, v47
	v_rcp_f32_e32 v48, v48
	v_rcp_f32_e32 v49, v49
	v_pk_mul_f32 v[38:39], v[38:39], s[100:101] op_sel:[0,1]
	v_pk_mul_f32 v[40:41], v[40:41], s[100:101] op_sel:[0,1]
	v_pk_mul_f32 v[38:39], v[38:39], v[46:47]
	v_pk_mul_f32 v[40:41], v[40:41], v[48:49]
	v_pk_mul_f32 v[38:39], v[38:39], v[98:99]
	v_pk_mul_f32 v[40:41], v[40:41], v[100:101]
	v_min_f32_e32 v34, 0x44e00000, v34
	v_min_f32_e32 v35, 0x44e00000, v35
	v_min_f32_e32 v36, 0x44e00000, v36
	v_min_f32_e32 v37, 0x44e00000, v37
	v_pk_mul_f32 v[46:47], v[34:35], s[100:101] op_sel_hi:[1,0]
	v_pk_mul_f32 v[48:49], v[36:37], s[100:101] op_sel_hi:[1,0]
	v_exp_f32_e32 v46, v46
	v_exp_f32_e32 v47, v47
	v_exp_f32_e32 v48, v48
	v_exp_f32_e32 v49, v49
	v_med3_f32 v102, v102, s81, v139
	v_med3_f32 v103, v103, s81, v139
	v_med3_f32 v104, v104, s81, v139
	v_med3_f32 v105, v105, s81, v139
	v_pk_add_f32 v[102:103], v[102:103], v[50:51]
	v_pk_add_f32 v[104:105], v[104:105], v[50:51]
	v_pk_add_f32 v[46:47], v[46:47], 1.0 op_sel_hi:[1,0]
	v_pk_add_f32 v[48:49], v[48:49], 1.0 op_sel_hi:[1,0]
	v_rcp_f32_e32 v46, v46
	v_rcp_f32_e32 v47, v47
	v_rcp_f32_e32 v48, v48
	v_rcp_f32_e32 v49, v49
	v_pk_mul_f32 v[34:35], v[34:35], s[100:101] op_sel:[0,1]
	v_pk_mul_f32 v[36:37], v[36:37], s[100:101] op_sel:[0,1]
	v_pk_mul_f32 v[34:35], v[34:35], v[46:47]
	v_pk_mul_f32 v[36:37], v[36:37], v[48:49]
	v_pk_mul_f32 v[34:35], v[34:35], v[102:103]
	v_pk_mul_f32 v[36:37], v[36:37], v[104:105]
	v_mov_b32_e32 v42, v131
	v_mov_b32_e32 v43, v131
	v_cvt_pk_fp8_f32 v42, v38, v39
	v_cvt_pk_fp8_f32 v43, v34, v35
	v_cvt_pk_fp8_f32 v42, v40, v41 op_sel:[0,0,1]
	v_cvt_pk_fp8_f32 v43, v36, v37 op_sel:[0,0,1]
	s_nop 0
	global_store_dwordx2 v[44:45], v[42:43], off sc1
	s_nop 1
	v_lshl_add_u64 v[44:45], v[134:135], 0, s[34:35]
	s_mov_b64 s[34:35], 0x50000
	v_min_f32_e32 v30, 0x44e00000, v30
	v_min_f32_e32 v31, 0x44e00000, v31
	v_min_f32_e32 v32, 0x44e00000, v32
	v_min_f32_e32 v33, 0x44e00000, v33
	v_pk_mul_f32 v[46:47], v[30:31], s[100:101] op_sel_hi:[1,0]
	v_pk_mul_f32 v[48:49], v[32:33], s[100:101] op_sel_hi:[1,0]
	v_exp_f32_e32 v46, v46
	v_exp_f32_e32 v47, v47
	v_exp_f32_e32 v48, v48
	v_exp_f32_e32 v49, v49
	v_med3_f32 v106, v106, s81, v139
	v_med3_f32 v107, v107, s81, v139
	v_med3_f32 v108, v108, s81, v139
	v_med3_f32 v109, v109, s81, v139
	v_pk_add_f32 v[106:107], v[106:107], v[50:51]
	v_pk_add_f32 v[108:109], v[108:109], v[50:51]
	v_pk_add_f32 v[46:47], v[46:47], 1.0 op_sel_hi:[1,0]
	v_pk_add_f32 v[48:49], v[48:49], 1.0 op_sel_hi:[1,0]
	v_rcp_f32_e32 v46, v46
	v_rcp_f32_e32 v47, v47
	v_rcp_f32_e32 v48, v48
	v_rcp_f32_e32 v49, v49
	v_pk_mul_f32 v[30:31], v[30:31], s[100:101] op_sel:[0,1]
	v_pk_mul_f32 v[32:33], v[32:33], s[100:101] op_sel:[0,1]
	v_pk_mul_f32 v[30:31], v[30:31], v[46:47]
	v_pk_mul_f32 v[32:33], v[32:33], v[48:49]
	v_pk_mul_f32 v[30:31], v[30:31], v[106:107]
	v_pk_mul_f32 v[32:33], v[32:33], v[108:109]
	v_min_f32_e32 v26, 0x44e00000, v26
	v_min_f32_e32 v27, 0x44e00000, v27
	v_min_f32_e32 v28, 0x44e00000, v28
	v_min_f32_e32 v29, 0x44e00000, v29
	v_pk_mul_f32 v[46:47], v[26:27], s[100:101] op_sel_hi:[1,0]
	v_pk_mul_f32 v[48:49], v[28:29], s[100:101] op_sel_hi:[1,0]
	v_exp_f32_e32 v46, v46
	v_exp_f32_e32 v47, v47
	v_exp_f32_e32 v48, v48
	v_exp_f32_e32 v49, v49
	v_med3_f32 v110, v110, s81, v139
	v_med3_f32 v111, v111, s81, v139
	v_med3_f32 v112, v112, s81, v139
	v_med3_f32 v113, v113, s81, v139
	v_pk_add_f32 v[110:111], v[110:111], v[50:51]
	v_pk_add_f32 v[112:113], v[112:113], v[50:51]
	v_pk_add_f32 v[46:47], v[46:47], 1.0 op_sel_hi:[1,0]
	v_pk_add_f32 v[48:49], v[48:49], 1.0 op_sel_hi:[1,0]
	v_rcp_f32_e32 v46, v46
	v_rcp_f32_e32 v47, v47
	v_rcp_f32_e32 v48, v48
	v_rcp_f32_e32 v49, v49
	v_pk_mul_f32 v[26:27], v[26:27], s[100:101] op_sel:[0,1]
	v_pk_mul_f32 v[28:29], v[28:29], s[100:101] op_sel:[0,1]
	v_pk_mul_f32 v[26:27], v[26:27], v[46:47]
	v_pk_mul_f32 v[28:29], v[28:29], v[48:49]
	v_pk_mul_f32 v[26:27], v[26:27], v[110:111]
	v_pk_mul_f32 v[28:29], v[28:29], v[112:113]
	v_mov_b32_e32 v42, v131
	v_mov_b32_e32 v43, v131
	v_cvt_pk_fp8_f32 v42, v30, v31
	v_cvt_pk_fp8_f32 v43, v26, v27
	v_cvt_pk_fp8_f32 v42, v32, v33 op_sel:[0,0,1]
	v_cvt_pk_fp8_f32 v43, v28, v29 op_sel:[0,0,1]
	s_nop 0
	global_store_dwordx2 v[44:45], v[42:43], off sc1
	s_nop 1
	v_lshl_add_u64 v[44:45], v[134:135], 0, s[34:35]
	s_mov_b64 s[34:35], 0x58000
	v_min_f32_e32 v22, 0x44e00000, v22
	v_min_f32_e32 v23, 0x44e00000, v23
	v_min_f32_e32 v24, 0x44e00000, v24
	v_min_f32_e32 v25, 0x44e00000, v25
	v_pk_mul_f32 v[46:47], v[22:23], s[100:101] op_sel_hi:[1,0]
	v_pk_mul_f32 v[48:49], v[24:25], s[100:101] op_sel_hi:[1,0]
	v_exp_f32_e32 v46, v46
	v_exp_f32_e32 v47, v47
	v_exp_f32_e32 v48, v48
	v_exp_f32_e32 v49, v49
	v_med3_f32 v114, v114, s81, v139
	v_med3_f32 v115, v115, s81, v139
	v_med3_f32 v116, v116, s81, v139
	v_med3_f32 v117, v117, s81, v139
	v_pk_add_f32 v[114:115], v[114:115], v[50:51]
	v_pk_add_f32 v[116:117], v[116:117], v[50:51]
	v_pk_add_f32 v[46:47], v[46:47], 1.0 op_sel_hi:[1,0]
	v_pk_add_f32 v[48:49], v[48:49], 1.0 op_sel_hi:[1,0]
	v_rcp_f32_e32 v46, v46
	v_rcp_f32_e32 v47, v47
	v_rcp_f32_e32 v48, v48
	v_rcp_f32_e32 v49, v49
	v_pk_mul_f32 v[22:23], v[22:23], s[100:101] op_sel:[0,1]
	v_pk_mul_f32 v[24:25], v[24:25], s[100:101] op_sel:[0,1]
	v_pk_mul_f32 v[22:23], v[22:23], v[46:47]
	v_pk_mul_f32 v[24:25], v[24:25], v[48:49]
	v_pk_mul_f32 v[22:23], v[22:23], v[114:115]
	v_pk_mul_f32 v[24:25], v[24:25], v[116:117]
	v_min_f32_e32 v220, 0x44e00000, v220
	v_min_f32_e32 v221, 0x44e00000, v221
	v_min_f32_e32 v222, 0x44e00000, v222
	v_min_f32_e32 v223, 0x44e00000, v223
	v_pk_mul_f32 v[46:47], v[220:221], s[100:101] op_sel_hi:[1,0]
	v_pk_mul_f32 v[48:49], v[222:223], s[100:101] op_sel_hi:[1,0]
	v_exp_f32_e32 v46, v46
	v_exp_f32_e32 v47, v47
	v_exp_f32_e32 v48, v48
	v_exp_f32_e32 v49, v49
	v_med3_f32 v118, v118, s81, v139
	v_med3_f32 v119, v119, s81, v139
	v_med3_f32 v120, v120, s81, v139
	v_med3_f32 v121, v121, s81, v139
	v_pk_add_f32 v[118:119], v[118:119], v[50:51]
	v_pk_add_f32 v[120:121], v[120:121], v[50:51]
	v_pk_add_f32 v[46:47], v[46:47], 1.0 op_sel_hi:[1,0]
	v_pk_add_f32 v[48:49], v[48:49], 1.0 op_sel_hi:[1,0]
	v_rcp_f32_e32 v46, v46
	v_rcp_f32_e32 v47, v47
	v_rcp_f32_e32 v48, v48
	v_rcp_f32_e32 v49, v49
	v_pk_mul_f32 v[220:221], v[220:221], s[100:101] op_sel:[0,1]
	v_pk_mul_f32 v[222:223], v[222:223], s[100:101] op_sel:[0,1]
	v_pk_mul_f32 v[220:221], v[220:221], v[46:47]
	v_pk_mul_f32 v[222:223], v[222:223], v[48:49]
	v_pk_mul_f32 v[220:221], v[220:221], v[118:119]
	v_pk_mul_f32 v[222:223], v[222:223], v[120:121]
	v_mov_b32_e32 v42, v131
	v_mov_b32_e32 v43, v131
	v_cvt_pk_fp8_f32 v42, v22, v23
	v_cvt_pk_fp8_f32 v43, v220, v221
	v_cvt_pk_fp8_f32 v42, v24, v25 op_sel:[0,0,1]
	v_cvt_pk_fp8_f32 v43, v222, v223 op_sel:[0,0,1]
	s_nop 0
	global_store_dwordx2 v[44:45], v[42:43], off sc1
	s_nop 1
	v_lshl_add_u64 v[44:45], v[134:135], 0, s[34:35]
	v_min_f32_e32 v2, 0x44e00000, v2
	v_min_f32_e32 v3, 0x44e00000, v3
	v_min_f32_e32 v4, 0x44e00000, v4
	v_min_f32_e32 v5, 0x44e00000, v5
	v_pk_mul_f32 v[46:47], v[2:3], s[100:101] op_sel_hi:[1,0]
	v_pk_mul_f32 v[48:49], v[4:5], s[100:101] op_sel_hi:[1,0]
	v_exp_f32_e32 v46, v46
	v_exp_f32_e32 v47, v47
	v_exp_f32_e32 v48, v48
	v_exp_f32_e32 v49, v49
	v_med3_f32 v122, v122, s81, v139
	v_med3_f32 v123, v123, s81, v139
	v_med3_f32 v124, v124, s81, v139
	v_med3_f32 v125, v125, s81, v139
	v_pk_add_f32 v[122:123], v[122:123], v[50:51]
	v_pk_add_f32 v[124:125], v[124:125], v[50:51]
	v_pk_add_f32 v[46:47], v[46:47], 1.0 op_sel_hi:[1,0]
	v_pk_add_f32 v[48:49], v[48:49], 1.0 op_sel_hi:[1,0]
	v_rcp_f32_e32 v46, v46
	v_rcp_f32_e32 v47, v47
	v_rcp_f32_e32 v48, v48
	v_rcp_f32_e32 v49, v49
	v_pk_mul_f32 v[2:3], v[2:3], s[100:101] op_sel:[0,1]
	v_pk_mul_f32 v[4:5], v[4:5], s[100:101] op_sel:[0,1]
	v_pk_mul_f32 v[2:3], v[2:3], v[46:47]
	v_pk_mul_f32 v[4:5], v[4:5], v[48:49]
	v_pk_mul_f32 v[2:3], v[2:3], v[122:123]
	v_pk_mul_f32 v[4:5], v[4:5], v[124:125]
	v_min_f32_e32 v10, 0x44e00000, v10
	v_min_f32_e32 v11, 0x44e00000, v11
	v_min_f32_e32 v12, 0x44e00000, v12
	v_min_f32_e32 v13, 0x44e00000, v13
	v_pk_mul_f32 v[46:47], v[10:11], s[100:101] op_sel_hi:[1,0]
	v_pk_mul_f32 v[48:49], v[12:13], s[100:101] op_sel_hi:[1,0]
	v_exp_f32_e32 v46, v46
	v_exp_f32_e32 v47, v47
	v_exp_f32_e32 v48, v48
	v_exp_f32_e32 v49, v49
	v_med3_f32 v126, v126, s81, v139
	v_med3_f32 v127, v127, s81, v139
	v_med3_f32 v128, v128, s81, v139
	v_med3_f32 v129, v129, s81, v139
	v_pk_add_f32 v[126:127], v[126:127], v[50:51]
	v_pk_add_f32 v[128:129], v[128:129], v[50:51]
	v_pk_add_f32 v[46:47], v[46:47], 1.0 op_sel_hi:[1,0]
	v_pk_add_f32 v[48:49], v[48:49], 1.0 op_sel_hi:[1,0]
	v_rcp_f32_e32 v46, v46
	v_rcp_f32_e32 v47, v47
	v_rcp_f32_e32 v48, v48
	v_rcp_f32_e32 v49, v49
	v_pk_mul_f32 v[10:11], v[10:11], s[100:101] op_sel:[0,1]
	v_pk_mul_f32 v[12:13], v[12:13], s[100:101] op_sel:[0,1]
	v_pk_mul_f32 v[10:11], v[10:11], v[46:47]
	v_pk_mul_f32 v[12:13], v[12:13], v[48:49]
	v_pk_mul_f32 v[10:11], v[10:11], v[126:127]
	v_pk_mul_f32 v[12:13], v[12:13], v[128:129]
	v_mov_b32_e32 v42, v131
	v_mov_b32_e32 v43, v131
	v_cvt_pk_fp8_f32 v42, v2, v3
	v_cvt_pk_fp8_f32 v43, v10, v11
	v_cvt_pk_fp8_f32 v42, v4, v5 op_sel:[0,0,1]
	v_cvt_pk_fp8_f32 v43, v12, v13 op_sel:[0,0,1]
	s_nop 0
	global_store_dwordx2 v[44:45], v[42:43], off sc1
	s_nop 1
	s_cbranch_vccnz .LBB0_1269
	v_readlane_b32 s88, v254, 4
	s_ashr_i32 s45, s44, 31
	v_readlane_b32 s92, v254, 8
	v_readlane_b32 s93, v254, 9
	s_lshl_b64 s[4:5], s[44:45], 14
	s_mov_b64 s[56:57], s[92:93]
	s_add_u32 s22, s56, s4
	v_mov_b32_e32 v2, v131
	s_addc_u32 s34, s57, s5
	s_lshl_b32 s4, s46, 7
	s_ashr_i32 s5, s4, 31
	v_mbcnt_lo_u32_b32 v2, -1, v2
	s_lshl_b64 s[4:5], s[4:5], 2
	v_mbcnt_hi_u32_b32 v2, -1, v2
	s_add_u32 s4, s22, s4
	s_addc_u32 s5, s34, s5
	s_lshl_b32 s22, s63, 2
	v_ashrrev_i32_e32 v2, 1, v2
	s_add_u32 s4, s4, s22
	v_and_b32_e32 v2, -8, v2
	s_addc_u32 s5, s5, 0
	v_ashrrev_i32_e32 v3, 31, v2
	v_lshl_add_u64 v[6:7], v[2:3], 2, s[4:5]
	v_lshl_add_u64 v[14:15], v[6:7], 0, s[6:7]
	global_load_dwordx4 v[10:13], v[6:7], off offset:16
	global_load_dwordx4 v[2:5], v[6:7], off
	v_add_co_u32_e32 v6, vcc, 0x2000, v6
	v_readlane_b32 s89, v254, 5
	s_nop 0
	v_addc_co_u32_e32 v7, vcc, 0, v7, vcc
	global_load_dwordx4 v[6:9], v[6:7], off
	s_nop 0
	global_load_dwordx4 v[14:17], v[14:15], off offset:16
	s_andn2_b64 vcc, exec, s[24:25]
	v_readlane_b32 s90, v254, 6
	v_readlane_b32 s91, v254, 7
	v_readlane_b32 s94, v254, 10
	v_readlane_b32 s95, v254, 11
	s_cbranch_vccnz .LBB0_1268
	s_barrier

.LBB0_1379:
	s_lshl_b32 s0, s71, 3
	s_add_i32 s0, s0, s72
	s_cmpk_gt_i32 s0, 0x1fff
	s_cbranch_scc1 .LBB0_1382
	s_add_u32 s11, s78, 0x500000
	s_addc_u32 s12, s79, 0
	v_lshlrev_b32_e32 v1, 3, v0
	s_add_u32 s13, s78, 0x580000
	s_waitcnt vmcnt(0)
	v_and_b32_e32 v40, 0x1f8, v1
	v_mov_b32_e32 v41, 0
	s_addc_u32 s14, s79, 0
	v_lshl_add_u64 v[8:9], s[78:79], 0, v[40:41]
	s_mov_b64 s[4:5], 0x26000000
	s_lshl_b32 s1, s71, 5
	s_lshl_b32 s3, s72, 2
	v_lshl_add_u64 v[42:43], v[8:9], 0, s[4:5]
	s_add_i32 s4, s1, s3
	s_ashr_i32 s1, s0, 31
	v_readlane_b32 s16, v254, 0
	s_lshl_b32 s2, s80, 3
	s_lshl_b32 s15, s80, 5
	s_lshl_b64 s[6:7], s[0:1], 13
	v_readlane_b32 s18, v254, 2
	v_and_b32_e32 v3, 63, v0
	v_readlane_b32 s19, v254, 3
	s_add_u32 s6, s18, s6
	v_lshlrev_b32_e32 v0, 5, v3
	v_mov_b32_e32 v1, v41
	s_addc_u32 s7, s19, s7
	v_lshl_add_u64 v[0:1], s[6:7], 0, v[0:1]
	s_mov_b64 s[6:7], 0x1000
	s_ashr_i32 s3, s2, 31
	v_lshl_add_u64 v[44:45], v[0:1], 0, s[6:7]
	s_lshl_b64 s[6:7], s[2:3], 13
	s_lshl_b64 s[8:9], s[0:1], 12
	s_add_u32 s8, s78, s8
	v_lshlrev_b32_e32 v0, 4, v3
	v_mov_b32_e32 v1, v41
	s_addc_u32 s9, s79, s9
	s_waitcnt lgkmcnt(1)
	v_or_b32_e32 v2, 0x200, v40
	s_waitcnt lgkmcnt(0)
	v_or_b32_e32 v4, 0x400, v40
	v_or_b32_e32 v6, 0x600, v40
	v_lshl_add_u64 v[0:1], s[8:9], 0, v[0:1]
	s_mov_b64 s[8:9], 0x18000000
	v_lshl_add_u64 v[46:47], v[0:1], 0, s[8:9]
	s_lshl_b64 s[8:9], s[2:3], 12
	s_add_i32 s1, 0, 0x24080
	v_lshlrev_b32_e32 v40, 2, v40
	v_lshlrev_b32_e32 v120, 2, v2
	v_lshlrev_b32_e32 v121, 2, v4
	v_lshlrev_b32_e32 v122, 2, v6
	s_mov_b32 s10, 0x3d800000
	v_readlane_b32 s17, v254, 1
	s_mov_b32 s22, s4
	s_ashr_i32 s23, s22, 31
	s_lshl_b64 s[24:25], s[22:23], 2
	s_add_u32 s26, s11, s24
	s_addc_u32 s27, s12, s25
	global_load_dwordx4 v[204:207], v41, s[26:27]
	s_add_u32 s26, s13, s24
	s_addc_u32 s27, s14, s25
	global_load_dwordx4 v[208:211], v41, s[26:27]
	s_add_i32 s22, s22, s15
	s_ashr_i32 s23, s22, 31
	s_lshl_b64 s[24:25], s[22:23], 2
	s_add_u32 s26, s11, s24
	s_addc_u32 s27, s12, s25
	global_load_dwordx4 v[212:215], v41, s[26:27]
	s_add_u32 s26, s13, s24
	s_addc_u32 s27, s14, s25
	global_load_dwordx4 v[216:219], v41, s[26:27]
	s_add_i32 s22, s22, s15
	s_ashr_i32 s23, s22, 31
	s_lshl_b64 s[24:25], s[22:23], 2
	s_add_u32 s26, s11, s24
	s_addc_u32 s27, s12, s25
	global_load_dwordx4 v[220:223], v41, s[26:27]
	s_add_u32 s26, s13, s24
	s_addc_u32 s27, s14, s25
	global_load_dwordx4 v[224:227], v41, s[26:27]
	s_add_i32 s22, s22, s15
	s_ashr_i32 s23, s22, 31
	s_lshl_b64 s[24:25], s[22:23], 2
	s_add_u32 s26, s11, s24
	s_addc_u32 s27, s12, s25
	global_load_dwordx4 v[228:231], v41, s[26:27]
	s_add_u32 s26, s13, s24
	s_addc_u32 s27, s14, s25
	global_load_dwordx4 v[232:235], v41, s[26:27]
	s_add_i32 s22, s22, s15
	s_waitcnt vmcnt(0)
.LBB0_1381:
	s_ashr_i32 s3, s0, 11
	s_mul_hi_i32 s5, s3, 0xc000
	s_mul_i32 s3, s3, 0xc000
	s_add_u32 s3, s78, s3
	s_addc_u32 s20, s79, s5
	s_ashr_i32 s5, s4, 31
	s_lshl_b64 s[16:17], s[4:5], 2
	s_add_u32 s18, s11, s16
	s_addc_u32 s19, s12, s17
	v_mov_b32_e32 v16, v204
	v_mov_b32_e32 v17, v205
	v_mov_b32_e32 v18, v206
	v_mov_b32_e32 v19, v207
	s_add_u32 s16, s13, s16
	s_addc_u32 s17, s14, s17
	v_mov_b32_e32 v27, v208
	s_add_i32 s18, s4, 1
	s_ashr_i32 s19, s18, 31
	s_lshl_b64 s[16:17], s[18:19], 2
	s_add_u32 s16, s13, s16
	s_addc_u32 s17, s14, s17
	v_mov_b32_e32 v24, v209
	v_mov_b32_e32 v25, v210
	v_mov_b32_e32 v26, v211
	v_mov_b32_e32 v204, v212
	v_mov_b32_e32 v205, v213
	v_mov_b32_e32 v206, v214
	v_mov_b32_e32 v207, v215
	v_mov_b32_e32 v208, v216
	v_mov_b32_e32 v209, v217
	v_mov_b32_e32 v210, v218
	v_mov_b32_e32 v211, v219
	v_mov_b32_e32 v212, v220
	v_mov_b32_e32 v213, v221
	v_mov_b32_e32 v214, v222
	v_mov_b32_e32 v215, v223
	v_mov_b32_e32 v216, v224
	v_mov_b32_e32 v217, v225
	v_mov_b32_e32 v218, v226
	v_mov_b32_e32 v219, v227
	v_mov_b32_e32 v220, v228
	v_mov_b32_e32 v221, v229
	v_mov_b32_e32 v222, v230
	v_mov_b32_e32 v223, v231
	v_mov_b32_e32 v224, v232
	v_mov_b32_e32 v225, v233
	v_mov_b32_e32 v226, v234
	v_mov_b32_e32 v227, v235
	global_load_dwordx4 v[52:55], v[46:47], off nt
	global_load_dwordx4 v[92:95], v[46:47], off offset:1024 nt
	global_load_dwordx4 v[36:39], v[46:47], off offset:2048 nt
	global_load_dwordx4 v[32:35], v[46:47], off offset:3072 nt
	s_add_u32 s16, s3, 0x40a000
	s_addc_u32 s17, s20, 0
	global_load_dwordx4 v[4:7], v40, s[16:17] offset:16
	global_load_dwordx4 v[12:15], v40, s[16:17]
	global_load_dwordx4 v[0:3], v120, s[16:17] offset:16
	global_load_dwordx4 v[8:11], v120, s[16:17]
	s_waitcnt vmcnt(10)
	v_lshlrev_b32_e32 v16, 2, v16
	v_lshlrev_b32_e32 v17, 2, v17
	v_lshlrev_b32_e32 v18, 2, v18
	v_lshlrev_b32_e32 v19, 2, v19
	v_add_u32_e32 v16, s1, v16
	v_add_u32_e32 v17, s1, v17
	v_add_u32_e32 v18, s1, v18
	v_add_u32_e32 v19, s1, v19
	ds_read_b32 v28, v16
	ds_read_b32 v29, v17
	ds_read_b32 v30, v18
	ds_read_b32 v31, v19
	global_load_dwordx4 v[16:19], v121, s[16:17] offset:16
	global_load_dwordx4 v[20:23], v121, s[16:17]
	s_waitcnt vmcnt(11) lgkmcnt(3)
	v_add_u32_e32 v28, v27, v28
	s_waitcnt vmcnt(10) lgkmcnt(2)
	v_add_u32_e32 v24, v24, v29
	s_waitcnt lgkmcnt(1)
	v_add_u32_e32 v30, v25, v30
	s_waitcnt lgkmcnt(0)
	v_add_u32_e32 v26, v26, v31
	v_ashrrev_i32_e32 v29, 31, v28
	v_ashrrev_i32_e32 v25, 31, v24
	v_ashrrev_i32_e32 v31, 31, v30
	v_ashrrev_i32_e32 v27, 31, v26
	v_lshlrev_b64 v[28:29], 11, v[28:29]
	v_lshlrev_b64 v[24:25], 11, v[24:25]
	v_lshlrev_b64 v[30:31], 11, v[30:31]
	v_lshlrev_b64 v[26:27], 11, v[26:27]
	v_lshl_add_u64 v[28:29], v[42:43], 0, v[28:29]
	v_lshl_add_u64 v[24:25], v[42:43], 0, v[24:25]
	v_lshl_add_u64 v[30:31], v[42:43], 0, v[30:31]
	v_lshl_add_u64 v[48:49], v[42:43], 0, v[26:27]
	global_load_dwordx2 v[50:51], v[28:29], off nt
	global_load_dwordx2 v[88:89], v[28:29], off offset:512 nt
	global_load_dwordx2 v[124:125], v[28:29], off offset:1024 nt
	global_load_dwordx2 v[118:119], v[28:29], off offset:1536 nt
	global_load_dwordx2 v[56:57], v[24:25], off nt
	global_load_dwordx2 v[90:91], v[24:25], off offset:512 nt
	global_load_dwordx2 v[126:127], v[24:25], off offset:1024 nt
	global_load_dwordx2 v[108:109], v[24:25], off offset:1536 nt
	global_load_dwordx2 v[58:59], v[30:31], off nt
	global_load_dwordx2 v[96:97], v[30:31], off offset:512 nt
	global_load_dwordx2 v[128:129], v[30:31], off offset:1024 nt
	global_load_dwordx2 v[104:105], v[30:31], off offset:1536 nt
	global_load_dwordx2 v[62:63], v[48:49], off nt
	global_load_dwordx2 v[102:103], v[48:49], off offset:512 nt
	global_load_dwordx2 v[130:131], v[48:49], off offset:1024 nt
	global_load_dwordx2 v[106:107], v[48:49], off offset:1536 nt
	global_load_dwordx4 v[24:27], v122, s[16:17] offset:16
	global_load_dwordx4 v[28:31], v122, s[16:17]
	s_waitcnt vmcnt(17)
	v_cvt_pk_f32_fp8_e32 v[80:81], v50
	v_cvt_pk_f32_fp8_sdwa v[82:83], v50 src0_sel:WORD_1
	v_cvt_pk_f32_fp8_e32 v[84:85], v51
	v_cvt_pk_f32_fp8_sdwa v[86:87], v51 src0_sel:WORD_1
	s_waitcnt vmcnt(13)
	v_cvt_pk_f32_fp8_e32 v[72:73], v56
	v_cvt_pk_f32_fp8_sdwa v[76:77], v56 src0_sel:WORD_1
	v_cvt_pk_f32_fp8_e32 v[132:133], v88
	v_cvt_pk_f32_fp8_sdwa v[134:135], v88 src0_sel:WORD_1
	v_cvt_pk_f32_fp8_e32 v[136:137], v89
	v_cvt_pk_f32_fp8_sdwa v[138:139], v89 src0_sel:WORD_1
	v_cvt_pk_f32_fp8_e32 v[148:149], v124
	v_cvt_pk_f32_fp8_sdwa v[150:151], v124 src0_sel:WORD_1
	v_cvt_pk_f32_fp8_e32 v[152:153], v125
	v_cvt_pk_f32_fp8_sdwa v[124:125], v125 src0_sel:WORD_1
	v_cvt_pk_f32_fp8_e32 v[176:177], v118
	v_cvt_pk_f32_fp8_sdwa v[178:179], v118 src0_sel:WORD_1
	v_cvt_pk_f32_fp8_e32 v[180:181], v119
	v_cvt_pk_f32_fp8_sdwa v[118:119], v119 src0_sel:WORD_1
	v_cvt_pk_f32_fp8_e32 v[74:75], v57
	v_cvt_pk_f32_fp8_sdwa v[78:79], v57 src0_sel:WORD_1
	s_waitcnt vmcnt(9)
	v_cvt_pk_f32_fp8_e32 v[64:65], v58
	v_cvt_pk_f32_fp8_sdwa v[66:67], v58 src0_sel:WORD_1
	v_cvt_pk_f32_fp8_e32 v[140:141], v90
	v_cvt_pk_f32_fp8_sdwa v[142:143], v90 src0_sel:WORD_1
	v_cvt_pk_f32_fp8_e32 v[144:145], v91
	v_cvt_pk_f32_fp8_sdwa v[146:147], v91 src0_sel:WORD_1
	v_cvt_pk_f32_fp8_e32 v[154:155], v126
	v_cvt_pk_f32_fp8_sdwa v[156:157], v126 src0_sel:WORD_1
	v_cvt_pk_f32_fp8_e32 v[158:159], v127
	v_cvt_pk_f32_fp8_sdwa v[126:127], v127 src0_sel:WORD_1
	v_cvt_pk_f32_fp8_e32 v[182:183], v108
	v_cvt_pk_f32_fp8_sdwa v[184:185], v108 src0_sel:WORD_1
	v_cvt_pk_f32_fp8_e32 v[186:187], v109
	v_cvt_pk_f32_fp8_sdwa v[108:109], v109 src0_sel:WORD_1
	v_cvt_pk_f32_fp8_e32 v[68:69], v59
	v_cvt_pk_f32_fp8_sdwa v[70:71], v59 src0_sel:WORD_1
	s_waitcnt vmcnt(5)
	v_cvt_pk_f32_fp8_e32 v[56:57], v62
	v_cvt_pk_f32_fp8_sdwa v[60:61], v62 src0_sel:WORD_1
	v_cvt_pk_f32_fp8_e32 v[110:111], v96
	v_cvt_pk_f32_fp8_sdwa v[112:113], v96 src0_sel:WORD_1
	v_cvt_pk_f32_fp8_e32 v[114:115], v97
	v_cvt_pk_f32_fp8_sdwa v[116:117], v97 src0_sel:WORD_1
	v_cvt_pk_f32_fp8_e32 v[160:161], v128
	v_cvt_pk_f32_fp8_sdwa v[162:163], v128 src0_sel:WORD_1
	v_cvt_pk_f32_fp8_e32 v[164:165], v129
	v_cvt_pk_f32_fp8_sdwa v[128:129], v129 src0_sel:WORD_1
	v_cvt_pk_f32_fp8_e32 v[188:189], v104
	v_cvt_pk_f32_fp8_sdwa v[190:191], v104 src0_sel:WORD_1
	v_cvt_pk_f32_fp8_e32 v[192:193], v105
	v_cvt_pk_f32_fp8_sdwa v[104:105], v105 src0_sel:WORD_1
	v_cvt_pk_f32_fp8_e32 v[58:59], v63
	v_cvt_pk_f32_fp8_sdwa v[62:63], v63 src0_sel:WORD_1
	s_waitcnt vmcnt(4)
	v_cvt_pk_f32_fp8_e32 v[96:97], v102
	v_cvt_pk_f32_fp8_sdwa v[100:101], v102 src0_sel:WORD_1
	v_cvt_pk_f32_fp8_e32 v[98:99], v103
	v_cvt_pk_f32_fp8_sdwa v[102:103], v103 src0_sel:WORD_1
	s_waitcnt vmcnt(3)
	v_cvt_pk_f32_fp8_e32 v[166:167], v130
	v_cvt_pk_f32_fp8_sdwa v[168:169], v130 src0_sel:WORD_1
	v_cvt_pk_f32_fp8_e32 v[170:171], v131
	v_cvt_pk_f32_fp8_sdwa v[130:131], v131 src0_sel:WORD_1
	s_waitcnt vmcnt(2)
	v_cvt_pk_f32_fp8_e32 v[194:195], v106
	v_cvt_pk_f32_fp8_sdwa v[196:197], v106 src0_sel:WORD_1
	v_cvt_pk_f32_fp8_e32 v[198:199], v107
	v_cvt_pk_f32_fp8_sdwa v[106:107], v107 src0_sel:WORD_1
	v_pk_add_f32 v[80:81], v[80:81], 0 op_sel_hi:[1,0]
	v_pk_add_f32 v[82:83], v[82:83], 0 op_sel_hi:[1,0]
	v_pk_add_f32 v[84:85], v[84:85], 0 op_sel_hi:[1,0]
	v_pk_add_f32 v[86:87], v[86:87], 0 op_sel_hi:[1,0]
	v_pk_add_f32 v[132:133], v[132:133], 0 op_sel_hi:[1,0]
	v_pk_add_f32 v[134:135], v[134:135], 0 op_sel_hi:[1,0]
	v_pk_add_f32 v[136:137], v[136:137], 0 op_sel_hi:[1,0]
	v_pk_add_f32 v[138:139], v[138:139], 0 op_sel_hi:[1,0]
	v_pk_add_f32 v[148:149], v[148:149], 0 op_sel_hi:[1,0]
	v_pk_add_f32 v[150:151], v[150:151], 0 op_sel_hi:[1,0]
	v_pk_add_f32 v[152:153], v[152:153], 0 op_sel_hi:[1,0]
	v_pk_add_f32 v[124:125], v[124:125], 0 op_sel_hi:[1,0]
	v_pk_add_f32 v[176:177], v[176:177], 0 op_sel_hi:[1,0]
	v_pk_add_f32 v[178:179], v[178:179], 0 op_sel_hi:[1,0]
	v_pk_add_f32 v[180:181], v[180:181], 0 op_sel_hi:[1,0]
	v_pk_add_f32 v[118:119], v[118:119], 0 op_sel_hi:[1,0]
	v_pk_add_f32 v[76:77], v[82:83], v[76:77]
	v_pk_add_f32 v[72:73], v[80:81], v[72:73]
	v_pk_add_f32 v[78:79], v[86:87], v[78:79]
	v_pk_add_f32 v[74:75], v[84:85], v[74:75]
	v_pk_add_f32 v[80:81], v[134:135], v[142:143]
	v_pk_add_f32 v[82:83], v[132:133], v[140:141]
	v_pk_add_f32 v[84:85], v[138:139], v[146:147]
	v_pk_add_f32 v[86:87], v[136:137], v[144:145]
	v_pk_add_f32 v[132:133], v[150:151], v[156:157]
	v_pk_add_f32 v[134:135], v[148:149], v[154:155]
	v_pk_add_f32 v[124:125], v[124:125], v[126:127]
	v_pk_add_f32 v[126:127], v[152:153], v[158:159]
	v_pk_add_f32 v[136:137], v[178:179], v[184:185]
	v_pk_add_f32 v[138:139], v[176:177], v[182:183]
	v_pk_add_f32 v[108:109], v[118:119], v[108:109]
	v_pk_add_f32 v[118:119], v[180:181], v[186:187]
	v_pk_add_f32 v[64:65], v[72:73], v[64:65]
	v_pk_add_f32 v[66:67], v[76:77], v[66:67]
	v_pk_add_f32 v[68:69], v[74:75], v[68:69]
	v_pk_add_f32 v[70:71], v[78:79], v[70:71]
	v_pk_add_f32 v[72:73], v[82:83], v[110:111]
	v_pk_add_f32 v[74:75], v[80:81], v[112:113]
	v_pk_add_f32 v[76:77], v[86:87], v[114:115]
	v_pk_add_f32 v[78:79], v[84:85], v[116:117]
	v_pk_add_f32 v[80:81], v[134:135], v[160:161]
	v_pk_add_f32 v[82:83], v[132:133], v[162:163]
	v_pk_add_f32 v[84:85], v[126:127], v[164:165]
	v_pk_add_f32 v[86:87], v[124:125], v[128:129]
	v_pk_add_f32 v[110:111], v[138:139], v[188:189]
	v_pk_add_f32 v[112:113], v[136:137], v[190:191]
	v_pk_add_f32 v[114:115], v[118:119], v[192:193]
	v_pk_add_f32 v[104:105], v[108:109], v[104:105]
	v_pk_add_f32 v[60:61], v[66:67], v[60:61]
	v_pk_add_f32 v[56:57], v[64:65], v[56:57]
	v_lshlrev_b32_e32 v48, 16, v52
	v_and_b32_e32 v49, 0xffff0000, v52
	v_lshlrev_b32_e32 v52, 16, v53
	v_and_b32_e32 v53, 0xffff0000, v53
	v_pk_add_f32 v[62:63], v[70:71], v[62:63]
	v_pk_add_f32 v[58:59], v[68:69], v[58:59]
	v_pk_add_f32 v[64:65], v[74:75], v[100:101]
	v_pk_add_f32 v[66:67], v[72:73], v[96:97]
	v_pk_add_f32 v[68:69], v[78:79], v[102:103]
	v_pk_add_f32 v[70:71], v[76:77], v[98:99]
	v_pk_add_f32 v[72:73], v[82:83], v[168:169]
	v_pk_add_f32 v[74:75], v[80:81], v[166:167]
	v_pk_add_f32 v[76:77], v[86:87], v[130:131]
	v_pk_add_f32 v[78:79], v[84:85], v[170:171]
	v_pk_add_f32 v[80:81], v[112:113], v[196:197]
	v_pk_add_f32 v[82:83], v[110:111], v[194:195]
	v_pk_add_f32 v[84:85], v[104:105], v[106:107]
	v_pk_add_f32 v[86:87], v[114:115], v[198:199]
	v_pk_mul_f32 v[56:57], v[56:57], s[10:11] op_sel_hi:[1,0]
	v_pk_mul_f32 v[60:61], v[60:61], s[10:11] op_sel_hi:[1,0]
	v_lshlrev_b32_e32 v50, 16, v54
	v_and_b32_e32 v51, 0xffff0000, v54
	v_lshlrev_b32_e32 v54, 16, v55
	v_and_b32_e32 v55, 0xffff0000, v55
	v_lshlrev_b32_e32 v88, 16, v92
	v_and_b32_e32 v89, 0xffff0000, v92
	v_lshlrev_b32_e32 v92, 16, v93
	v_and_b32_e32 v93, 0xffff0000, v93
	v_lshlrev_b32_e32 v90, 16, v94
	v_and_b32_e32 v91, 0xffff0000, v94
	v_lshlrev_b32_e32 v94, 16, v95
	v_and_b32_e32 v95, 0xffff0000, v95
	v_lshlrev_b32_e32 v172, 16, v36
	v_and_b32_e32 v173, 0xffff0000, v36
	v_lshlrev_b32_e32 v36, 16, v37
	v_and_b32_e32 v37, 0xffff0000, v37
	v_lshlrev_b32_e32 v174, 16, v38
	v_and_b32_e32 v175, 0xffff0000, v38
	v_lshlrev_b32_e32 v38, 16, v39
	v_and_b32_e32 v39, 0xffff0000, v39
	v_lshlrev_b32_e32 v200, 16, v32
	v_and_b32_e32 v201, 0xffff0000, v32
	v_lshlrev_b32_e32 v32, 16, v33
	v_and_b32_e32 v33, 0xffff0000, v33
	v_lshlrev_b32_e32 v202, 16, v34
	v_and_b32_e32 v203, 0xffff0000, v34
	v_lshlrev_b32_e32 v34, 16, v35
	v_and_b32_e32 v35, 0xffff0000, v35
	s_add_i32 s0, s0, s2
	s_add_i32 s4, s4, s15
	v_pk_mul_f32 v[58:59], v[58:59], s[10:11] op_sel_hi:[1,0]
	v_pk_mul_f32 v[62:63], v[62:63], s[10:11] op_sel_hi:[1,0]
	v_pk_mul_f32 v[66:67], v[66:67], s[10:11] op_sel_hi:[1,0]
	v_pk_mul_f32 v[64:65], v[64:65], s[10:11] op_sel_hi:[1,0]
	v_pk_mul_f32 v[70:71], v[70:71], s[10:11] op_sel_hi:[1,0]
	v_pk_mul_f32 v[68:69], v[68:69], s[10:11] op_sel_hi:[1,0]
	v_pk_mul_f32 v[74:75], v[74:75], s[10:11] op_sel_hi:[1,0]
	v_pk_mul_f32 v[72:73], v[72:73], s[10:11] op_sel_hi:[1,0]
	v_pk_mul_f32 v[78:79], v[78:79], s[10:11] op_sel_hi:[1,0]
	v_pk_mul_f32 v[76:77], v[76:77], s[10:11] op_sel_hi:[1,0]
	v_pk_mul_f32 v[82:83], v[82:83], s[10:11] op_sel_hi:[1,0]
	v_pk_mul_f32 v[80:81], v[80:81], s[10:11] op_sel_hi:[1,0]
	v_pk_mul_f32 v[86:87], v[86:87], s[10:11] op_sel_hi:[1,0]
	v_pk_mul_f32 v[84:85], v[84:85], s[10:11] op_sel_hi:[1,0]
	v_pk_fma_f32 v[14:15], v[14:15], v[60:61], v[52:53]
	v_pk_fma_f32 v[12:13], v[12:13], v[56:57], v[48:49]
	v_lshl_add_u64 v[46:47], v[46:47], 0, s[8:9]
	s_cmpk_lt_i32 s0, 0x2000
	v_pk_fma_f32 v[6:7], v[6:7], v[62:63], v[54:55]
	v_pk_fma_f32 v[4:5], v[4:5], v[58:59], v[50:51]
	v_pk_fma_f32 v[10:11], v[10:11], v[64:65], v[92:93]
	v_pk_fma_f32 v[8:9], v[8:9], v[66:67], v[88:89]
	v_pk_fma_f32 v[2:3], v[2:3], v[68:69], v[94:95]
	v_pk_fma_f32 v[0:1], v[0:1], v[70:71], v[90:91]
	v_pk_fma_f32 v[22:23], v[22:23], v[72:73], v[36:37]
	v_pk_fma_f32 v[20:21], v[20:21], v[74:75], v[172:173]
	v_pk_fma_f32 v[18:19], v[18:19], v[76:77], v[38:39]
	v_pk_fma_f32 v[16:17], v[16:17], v[78:79], v[174:175]
	s_waitcnt vmcnt(0)
	v_pk_fma_f32 v[30:31], v[30:31], v[80:81], v[32:33]
	v_pk_fma_f32 v[28:29], v[28:29], v[82:83], v[200:201]
	v_pk_fma_f32 v[26:27], v[26:27], v[84:85], v[34:35]
	v_pk_fma_f32 v[24:25], v[24:25], v[86:87], v[202:203]
	global_store_dwordx4 v[44:45], v[12:15], off offset:-4096 nt
	global_store_dwordx4 v[44:45], v[4:7], off offset:-4080 nt
	global_store_dwordx4 v[44:45], v[8:11], off offset:-2048 nt
	global_store_dwordx4 v[44:45], v[0:3], off offset:-2032 nt
	global_store_dwordx4 v[44:45], v[20:23], off nt
	global_store_dwordx4 v[44:45], v[16:19], off offset:16 nt
	global_store_dwordx4 v[44:45], v[28:31], off offset:2048 nt
	global_store_dwordx4 v[44:45], v[24:27], off offset:2064 nt
	v_lshl_add_u64 v[44:45], v[44:45], 0, s[6:7]
	s_cbranch_scc1 .LBB0_1381
